# weight-conversion inner loops: both 16-load batches of an item issued before the first wait (32 loads in flight), on top of v040
# speedup vs baseline: 1.0007x; 1.0000x over previous
.LBB0_57:
	s_lshl_b32 s27, s8, 1
	s_lshl_b32 s30, s20, 1
	v_or_b32_e32 v21, s27, v1
	v_or_b32_e32 v31, s30, v6
	s_add_i32 s31, s27, 4
	s_add_i32 s41, s30, 4
	s_add_i32 s49, s27, 8
	s_add_i32 s50, s30, 8
	s_add_i32 s51, s27, 12
	s_add_i32 s52, s30, 12
	s_add_i32 s53, s27, 16
	s_add_i32 s54, s30, 16
	s_add_i32 s55, s27, 20
	s_add_i32 s56, s30, 20
	s_add_i32 s57, s27, 24
	s_add_i32 s58, s30, 24
	s_add_i32 s27, s27, 28
	s_add_i32 s30, s30, 28
	v_add_u32_e32 v33, s5, v21
	v_add_u32_e32 v4, s26, v31
	v_or_b32_e32 v35, s31, v1
	v_or_b32_e32 v37, s41, v6
	v_or_b32_e32 v39, s49, v1
	v_or_b32_e32 v41, s50, v6
	v_or_b32_e32 v43, s51, v1
	v_or_b32_e32 v47, s52, v6
	v_or_b32_e32 v49, s53, v1
	v_or_b32_e32 v51, s54, v6
	v_or_b32_e32 v53, s55, v1
	v_or_b32_e32 v88, s56, v6
	v_or_b32_e32 v89, s57, v1
	v_or_b32_e32 v90, s58, v6
	v_or_b32_e32 v91, s27, v1
	v_or_b32_e32 v92, s30, v6
	v_mad_i64_i32 v[4:5], s[30:31], v4, s44, v[2:3]
	v_mad_i64_i32 v[54:55], s[30:31], v33, s44, v[2:3]
	v_add_u32_e32 v33, s5, v35
	v_add_u32_e32 v56, s26, v37
	v_add_u32_e32 v66, s5, v39
	v_add_u32_e32 v64, s26, v41
	v_add_u32_e32 v70, s5, v43
	v_add_u32_e32 v68, s26, v47
	v_add_u32_e32 v74, s5, v49
	v_add_u32_e32 v72, s26, v51
	v_add_u32_e32 v78, s5, v53
	v_add_u32_e32 v76, s26, v88
	v_add_u32_e32 v82, s5, v89
	v_add_u32_e32 v80, s26, v90
	v_add_u32_e32 v86, s5, v91
	v_add_u32_e32 v84, s26, v92
	v_mad_i64_i32 v[56:57], s[30:31], v56, s44, v[2:3]
	v_mad_i64_i32 v[58:59], s[30:31], v33, s44, v[2:3]
	v_mad_i64_i32 v[64:65], s[30:31], v64, s44, v[2:3]
	v_mad_i64_i32 v[66:67], s[30:31], v66, s44, v[2:3]
	v_mad_i64_i32 v[68:69], s[30:31], v68, s44, v[2:3]
	v_mad_i64_i32 v[70:71], s[30:31], v70, s44, v[2:3]
	v_mad_i64_i32 v[72:73], s[30:31], v72, s44, v[2:3]
	v_mad_i64_i32 v[74:75], s[30:31], v74, s44, v[2:3]
	v_mad_i64_i32 v[76:77], s[30:31], v76, s44, v[2:3]
	v_mad_i64_i32 v[78:79], s[30:31], v78, s44, v[2:3]
	v_mad_i64_i32 v[80:81], s[30:31], v80, s44, v[2:3]
	v_mad_i64_i32 v[82:83], s[30:31], v82, s44, v[2:3]
	v_mad_i64_i32 v[84:85], s[30:31], v84, s44, v[2:3]
	v_mad_i64_i32 v[86:87], s[30:31], v86, s44, v[2:3]
	global_load_dword v33, v[4:5], off
	global_load_dword v93, v[54:55], off
	global_load_dword v94, v[56:57], off
	global_load_dword v95, v[58:59], off
	global_load_dword v96, v[64:65], off
	global_load_dword v97, v[66:67], off
	global_load_dword v98, v[68:69], off
	global_load_dword v99, v[70:71], off
	global_load_dword v100, v[72:73], off
	global_load_dword v101, v[74:75], off
	global_load_dword v102, v[76:77], off
	global_load_dword v103, v[78:79], off
	global_load_dword v104, v[80:81], off
	global_load_dword v105, v[82:83], off
	global_load_dword v106, v[84:85], off
	global_load_dword v107, v[86:87], off
	s_add_i32 s20, s20, 16
	s_add_i32 s8, s8, 16
	s_add_i32 s21, s21, -16
	v_mad_u64_u32 v[4:5], s[30:31], v31, s43, v[10:11]
	s_cmp_lg_u32 s21, 0
	v_mad_u64_u32 v[54:55], s[30:31], v21, s43, v[10:11]
	v_mad_u64_u32 v[56:57], s[30:31], v37, s43, v[10:11]
	v_mad_u64_u32 v[58:59], s[30:31], v35, s43, v[10:11]
	v_mad_u64_u32 v[64:65], s[30:31], v41, s43, v[10:11]
	v_mad_u64_u32 v[66:67], s[30:31], v39, s43, v[10:11]
	v_mad_u64_u32 v[68:69], s[30:31], v47, s43, v[10:11]
	v_mad_u64_u32 v[70:71], s[30:31], v43, s43, v[10:11]
	v_mad_u64_u32 v[72:73], s[30:31], v51, s43, v[10:11]
	v_mad_u64_u32 v[74:75], s[30:31], v49, s43, v[10:11]
	v_mad_u64_u32 v[76:77], s[30:31], v88, s43, v[10:11]
	v_mad_u64_u32 v[78:79], s[30:31], v53, s43, v[10:11]
	v_mad_u64_u32 v[80:81], s[30:31], v90, s43, v[10:11]
	v_mad_u64_u32 v[82:83], s[30:31], v89, s43, v[10:11]
	v_mad_u64_u32 v[84:85], s[30:31], v92, s43, v[10:11]
	v_mad_u64_u32 v[86:87], s[30:31], v91, s43, v[10:11]
	s_lshl_b32 s27, s8, 1
	s_lshl_b32 s30, s20, 1
	v_or_b32_e32 v112, s27, v1
	v_or_b32_e32 v113, s30, v6
	s_add_i32 s31, s27, 4
	s_add_i32 s41, s30, 4
	s_add_i32 s49, s27, 8
	s_add_i32 s50, s30, 8
	s_add_i32 s51, s27, 12
	s_add_i32 s52, s30, 12
	s_add_i32 s53, s27, 16
	s_add_i32 s54, s30, 16
	s_add_i32 s55, s27, 20
	s_add_i32 s56, s30, 20
	s_add_i32 s57, s27, 24
	s_add_i32 s58, s30, 24
	s_add_i32 s27, s27, 28
	s_add_i32 s30, s30, 28
	v_add_u32_e32 v114, s5, v112
	v_add_u32_e32 v110, s26, v113
	v_or_b32_e32 v115, s31, v1
	v_or_b32_e32 v116, s41, v6
	v_or_b32_e32 v117, s49, v1
	v_or_b32_e32 v118, s50, v6
	v_or_b32_e32 v119, s51, v1
	v_or_b32_e32 v120, s52, v6
	v_or_b32_e32 v121, s53, v1
	v_or_b32_e32 v122, s54, v6
	v_or_b32_e32 v123, s55, v1
	v_or_b32_e32 v154, s56, v6
	v_or_b32_e32 v155, s57, v1
	v_or_b32_e32 v156, s58, v6
	v_or_b32_e32 v157, s27, v1
	v_or_b32_e32 v158, s30, v6
	v_mad_i64_i32 v[110:111], s[30:31], v110, s44, v[2:3]
	v_mad_i64_i32 v[124:125], s[30:31], v114, s44, v[2:3]
	v_add_u32_e32 v114, s5, v115
	v_add_u32_e32 v126, s26, v116
	v_add_u32_e32 v132, s5, v117
	v_add_u32_e32 v130, s26, v118
	v_add_u32_e32 v136, s5, v119
	v_add_u32_e32 v134, s26, v120
	v_add_u32_e32 v140, s5, v121
	v_add_u32_e32 v138, s26, v122
	v_add_u32_e32 v144, s5, v123
	v_add_u32_e32 v142, s26, v154
	v_add_u32_e32 v148, s5, v155
	v_add_u32_e32 v146, s26, v156
	v_add_u32_e32 v152, s5, v157
	v_add_u32_e32 v150, s26, v158
	v_mad_i64_i32 v[126:127], s[30:31], v126, s44, v[2:3]
	v_mad_i64_i32 v[128:129], s[30:31], v114, s44, v[2:3]
	v_mad_i64_i32 v[130:131], s[30:31], v130, s44, v[2:3]
	v_mad_i64_i32 v[132:133], s[30:31], v132, s44, v[2:3]
	v_mad_i64_i32 v[134:135], s[30:31], v134, s44, v[2:3]
	v_mad_i64_i32 v[136:137], s[30:31], v136, s44, v[2:3]
	v_mad_i64_i32 v[138:139], s[30:31], v138, s44, v[2:3]
	v_mad_i64_i32 v[140:141], s[30:31], v140, s44, v[2:3]
	v_mad_i64_i32 v[142:143], s[30:31], v142, s44, v[2:3]
	v_mad_i64_i32 v[144:145], s[30:31], v144, s44, v[2:3]
	v_mad_i64_i32 v[146:147], s[30:31], v146, s44, v[2:3]
	v_mad_i64_i32 v[148:149], s[30:31], v148, s44, v[2:3]
	v_mad_i64_i32 v[150:151], s[30:31], v150, s44, v[2:3]
	v_mad_i64_i32 v[152:153], s[30:31], v152, s44, v[2:3]
	global_load_dword v114, v[110:111], off
	global_load_dword v159, v[124:125], off
	global_load_dword v160, v[126:127], off
	global_load_dword v161, v[128:129], off
	global_load_dword v162, v[130:131], off
	global_load_dword v163, v[132:133], off
	global_load_dword v164, v[134:135], off
	global_load_dword v165, v[136:137], off
	global_load_dword v166, v[138:139], off
	global_load_dword v167, v[140:141], off
	global_load_dword v168, v[142:143], off
	global_load_dword v169, v[144:145], off
	global_load_dword v170, v[146:147], off
	global_load_dword v171, v[148:149], off
	global_load_dword v172, v[150:151], off
	global_load_dword v173, v[152:153], off
	s_add_i32 s20, s20, 16
	s_add_i32 s8, s8, 16
	s_add_i32 s21, s21, -16
	v_mad_u64_u32 v[110:111], s[30:31], v113, s43, v[10:11]
	s_cmp_lg_u32 s21, 0
	v_mad_u64_u32 v[124:125], s[30:31], v112, s43, v[10:11]
	v_mad_u64_u32 v[126:127], s[30:31], v116, s43, v[10:11]
	v_mad_u64_u32 v[128:129], s[30:31], v115, s43, v[10:11]
	v_mad_u64_u32 v[130:131], s[30:31], v118, s43, v[10:11]
	v_mad_u64_u32 v[132:133], s[30:31], v117, s43, v[10:11]
	v_mad_u64_u32 v[134:135], s[30:31], v120, s43, v[10:11]
	v_mad_u64_u32 v[136:137], s[30:31], v119, s43, v[10:11]
	v_mad_u64_u32 v[138:139], s[30:31], v122, s43, v[10:11]
	v_mad_u64_u32 v[140:141], s[30:31], v121, s43, v[10:11]
	v_mad_u64_u32 v[142:143], s[30:31], v154, s43, v[10:11]
	v_mad_u64_u32 v[144:145], s[30:31], v123, s43, v[10:11]
	v_mad_u64_u32 v[146:147], s[30:31], v156, s43, v[10:11]
	v_mad_u64_u32 v[148:149], s[30:31], v155, s43, v[10:11]
	v_mad_u64_u32 v[150:151], s[30:31], v158, s43, v[10:11]
	v_mad_u64_u32 v[152:153], s[30:31], v157, s43, v[10:11]
	s_waitcnt vmcnt(31)
	ds_write_b32 v4, v33
	s_waitcnt vmcnt(30)
	ds_write_b32 v54, v93
	s_waitcnt vmcnt(29)
	ds_write_b32 v56, v94
	s_waitcnt vmcnt(28)
	ds_write_b32 v58, v95
	s_waitcnt vmcnt(27)
	ds_write_b32 v64, v96
	s_waitcnt vmcnt(26)
	ds_write_b32 v66, v97
	s_waitcnt vmcnt(25)
	ds_write_b32 v68, v98
	s_waitcnt vmcnt(24)
	ds_write_b32 v70, v99
	s_waitcnt vmcnt(23)
	ds_write_b32 v72, v100
	s_waitcnt vmcnt(22)
	ds_write_b32 v74, v101
	s_waitcnt vmcnt(21)
	ds_write_b32 v76, v102
	s_waitcnt vmcnt(20)
	ds_write_b32 v78, v103
	s_waitcnt vmcnt(19)
	ds_write_b32 v80, v104
	s_waitcnt vmcnt(18)
	ds_write_b32 v82, v105
	s_waitcnt vmcnt(17)
	ds_write_b32 v84, v106
	s_waitcnt vmcnt(16)
	ds_write_b32 v86, v107
	s_waitcnt vmcnt(15)
	ds_write_b32 v110, v114
	s_waitcnt vmcnt(14)
	ds_write_b32 v124, v159
	s_waitcnt vmcnt(13)
	ds_write_b32 v126, v160
	s_waitcnt vmcnt(12)
	ds_write_b32 v128, v161
	s_waitcnt vmcnt(11)
	ds_write_b32 v130, v162
	s_waitcnt vmcnt(10)
	ds_write_b32 v132, v163
	s_waitcnt vmcnt(9)
	ds_write_b32 v134, v164
	s_waitcnt vmcnt(8)
	ds_write_b32 v136, v165
	s_waitcnt vmcnt(7)
	ds_write_b32 v138, v166
	s_waitcnt vmcnt(6)
	ds_write_b32 v140, v167
	s_waitcnt vmcnt(5)
	ds_write_b32 v142, v168
	s_waitcnt vmcnt(4)
	ds_write_b32 v144, v169
	s_waitcnt vmcnt(3)
	ds_write_b32 v146, v170
	s_waitcnt vmcnt(2)
	ds_write_b32 v148, v171
	s_waitcnt vmcnt(1)
	ds_write_b32 v150, v172
	s_waitcnt vmcnt(0)
	ds_write_b32 v152, v173

.LBB0_141:
	s_lshl_b32 s38, s21, 1
	s_lshl_b32 s39, s31, 1
	v_or_b32_e32 v21, s38, v1
	v_or_b32_e32 v31, s39, v6
	s_add_i32 s40, s38, 4
	s_add_i32 s41, s39, 4
	s_add_i32 s49, s38, 8
	s_add_i32 s50, s39, 8
	s_add_i32 s51, s38, 12
	s_add_i32 s52, s39, 12
	s_add_i32 s53, s38, 16
	s_add_i32 s54, s39, 16
	s_add_i32 s55, s38, 20
	s_add_i32 s56, s39, 20
	s_add_i32 s57, s38, 24
	s_add_i32 s58, s39, 24
	s_add_i32 s38, s38, 28
	s_add_i32 s39, s39, 28
	v_add_u32_e32 v56, s34, v31
	v_or_b32_e32 v33, s40, v1
	v_or_b32_e32 v35, s41, v6
	v_or_b32_e32 v37, s49, v1
	v_or_b32_e32 v39, s50, v6
	v_or_b32_e32 v41, s51, v1
	v_or_b32_e32 v43, s52, v6
	v_or_b32_e32 v47, s53, v1
	v_or_b32_e32 v49, s54, v6
	v_or_b32_e32 v51, s55, v1
	v_or_b32_e32 v53, s56, v6
	v_or_b32_e32 v90, s57, v1
	v_or_b32_e32 v91, s58, v6
	v_or_b32_e32 v92, s38, v1
	v_or_b32_e32 v93, s39, v6
	v_add_u32_e32 v4, s20, v21
	v_ashrrev_i32_e32 v57, 31, v56
	v_add_u32_e32 v58, s20, v33
	v_add_u32_e32 v64, s34, v35
	v_add_u32_e32 v66, s20, v37
	v_add_u32_e32 v68, s34, v39
	v_add_u32_e32 v70, s20, v41
	v_add_u32_e32 v72, s34, v43
	v_add_u32_e32 v74, s20, v47
	v_add_u32_e32 v76, s34, v49
	v_add_u32_e32 v78, s20, v51
	v_add_u32_e32 v80, s34, v53
	v_add_u32_e32 v82, s20, v90
	v_add_u32_e32 v84, s34, v91
	v_add_u32_e32 v86, s20, v92
	v_add_u32_e32 v88, s34, v93
	v_ashrrev_i32_e32 v5, 31, v4
	v_lshlrev_b64 v[56:57], 12, v[56:57]
	v_ashrrev_i32_e32 v65, 31, v64
	v_ashrrev_i32_e32 v59, 31, v58
	v_ashrrev_i32_e32 v69, 31, v68
	v_ashrrev_i32_e32 v67, 31, v66
	v_ashrrev_i32_e32 v73, 31, v72
	v_ashrrev_i32_e32 v71, 31, v70
	v_ashrrev_i32_e32 v77, 31, v76
	v_ashrrev_i32_e32 v75, 31, v74
	v_ashrrev_i32_e32 v81, 31, v80
	v_ashrrev_i32_e32 v79, 31, v78
	v_ashrrev_i32_e32 v85, 31, v84
	v_ashrrev_i32_e32 v83, 31, v82
	v_ashrrev_i32_e32 v89, 31, v88
	v_ashrrev_i32_e32 v87, 31, v86
	v_lshlrev_b64 v[4:5], 12, v[4:5]
	v_lshl_add_u64 v[56:57], v[2:3], 0, v[56:57]
	v_lshlrev_b64 v[58:59], 12, v[58:59]
	v_lshlrev_b64 v[64:65], 12, v[64:65]
	v_lshlrev_b64 v[66:67], 12, v[66:67]
	v_lshlrev_b64 v[68:69], 12, v[68:69]
	v_lshlrev_b64 v[70:71], 12, v[70:71]
	v_lshlrev_b64 v[72:73], 12, v[72:73]
	v_lshlrev_b64 v[74:75], 12, v[74:75]
	v_lshlrev_b64 v[76:77], 12, v[76:77]
	v_lshlrev_b64 v[78:79], 12, v[78:79]
	v_lshlrev_b64 v[80:81], 12, v[80:81]
	v_lshlrev_b64 v[82:83], 12, v[82:83]
	v_lshlrev_b64 v[84:85], 12, v[84:85]
	v_lshlrev_b64 v[86:87], 12, v[86:87]
	v_lshlrev_b64 v[88:89], 12, v[88:89]
	v_lshl_add_u64 v[4:5], v[2:3], 0, v[4:5]
	v_lshl_add_u64 v[64:65], v[2:3], 0, v[64:65]
	v_lshl_add_u64 v[58:59], v[2:3], 0, v[58:59]
	v_lshl_add_u64 v[68:69], v[2:3], 0, v[68:69]
	v_lshl_add_u64 v[66:67], v[2:3], 0, v[66:67]
	v_lshl_add_u64 v[72:73], v[2:3], 0, v[72:73]
	v_lshl_add_u64 v[70:71], v[2:3], 0, v[70:71]
	v_lshl_add_u64 v[76:77], v[2:3], 0, v[76:77]
	v_lshl_add_u64 v[74:75], v[2:3], 0, v[74:75]
	v_lshl_add_u64 v[80:81], v[2:3], 0, v[80:81]
	v_lshl_add_u64 v[78:79], v[2:3], 0, v[78:79]
	v_lshl_add_u64 v[84:85], v[2:3], 0, v[84:85]
	v_lshl_add_u64 v[82:83], v[2:3], 0, v[82:83]
	v_lshl_add_u64 v[88:89], v[2:3], 0, v[88:89]
	v_lshl_add_u64 v[86:87], v[2:3], 0, v[86:87]
	global_load_dword v94, v[56:57], off
	global_load_dword v95, v[4:5], off
	global_load_dword v96, v[64:65], off
	global_load_dword v97, v[58:59], off
	global_load_dword v98, v[68:69], off
	global_load_dword v99, v[66:67], off
	global_load_dword v100, v[72:73], off
	global_load_dword v101, v[70:71], off
	global_load_dword v102, v[76:77], off
	global_load_dword v103, v[74:75], off
	global_load_dword v104, v[80:81], off
	global_load_dword v105, v[78:79], off
	global_load_dword v106, v[84:85], off
	global_load_dword v107, v[82:83], off
	global_load_dword v108, v[88:89], off
	global_load_dword v109, v[86:87], off
	s_add_i32 s31, s31, 16
	s_add_i32 s21, s21, 16
	s_add_i32 s35, s35, -16
	v_mad_u64_u32 v[4:5], s[38:39], v31, s43, v[10:11]
	s_cmp_lg_u32 s35, 0
	v_mad_u64_u32 v[56:57], s[38:39], v21, s43, v[10:11]
	v_mad_u64_u32 v[58:59], s[38:39], v35, s43, v[10:11]
	v_mad_u64_u32 v[64:65], s[38:39], v33, s43, v[10:11]
	v_mad_u64_u32 v[66:67], s[38:39], v39, s43, v[10:11]
	v_mad_u64_u32 v[68:69], s[38:39], v37, s43, v[10:11]
	v_mad_u64_u32 v[70:71], s[38:39], v43, s43, v[10:11]
	v_mad_u64_u32 v[72:73], s[38:39], v41, s43, v[10:11]
	v_mad_u64_u32 v[74:75], s[38:39], v49, s43, v[10:11]
	v_mad_u64_u32 v[76:77], s[38:39], v47, s43, v[10:11]
	v_mad_u64_u32 v[78:79], s[38:39], v53, s43, v[10:11]
	v_mad_u64_u32 v[80:81], s[38:39], v51, s43, v[10:11]
	v_mad_u64_u32 v[82:83], s[38:39], v91, s43, v[10:11]
	v_mad_u64_u32 v[84:85], s[38:39], v90, s43, v[10:11]
	v_mad_u64_u32 v[86:87], s[38:39], v93, s43, v[10:11]
	v_mad_u64_u32 v[88:89], s[38:39], v92, s43, v[10:11]
	s_lshl_b32 s38, s21, 1
	s_lshl_b32 s39, s31, 1
	v_or_b32_e32 v112, s38, v1
	v_or_b32_e32 v113, s39, v6
	s_add_i32 s40, s38, 4
	s_add_i32 s41, s39, 4
	s_add_i32 s49, s38, 8
	s_add_i32 s50, s39, 8
	s_add_i32 s51, s38, 12
	s_add_i32 s52, s39, 12
	s_add_i32 s53, s38, 16
	s_add_i32 s54, s39, 16
	s_add_i32 s55, s38, 20
	s_add_i32 s56, s39, 20
	s_add_i32 s57, s38, 24
	s_add_i32 s58, s39, 24
	s_add_i32 s38, s38, 28
	s_add_i32 s39, s39, 28
	v_add_u32_e32 v124, s34, v113
	v_or_b32_e32 v114, s40, v1
	v_or_b32_e32 v115, s41, v6
	v_or_b32_e32 v116, s49, v1
	v_or_b32_e32 v117, s50, v6
	v_or_b32_e32 v118, s51, v1
	v_or_b32_e32 v119, s52, v6
	v_or_b32_e32 v120, s53, v1
	v_or_b32_e32 v121, s54, v6
	v_or_b32_e32 v122, s55, v1
	v_or_b32_e32 v123, s56, v6
	v_or_b32_e32 v154, s57, v1
	v_or_b32_e32 v155, s58, v6
	v_or_b32_e32 v156, s38, v1
	v_or_b32_e32 v157, s39, v6
	v_add_u32_e32 v110, s20, v112
	v_ashrrev_i32_e32 v125, 31, v124
	v_add_u32_e32 v126, s20, v114
	v_add_u32_e32 v128, s34, v115
	v_add_u32_e32 v130, s20, v116
	v_add_u32_e32 v132, s34, v117
	v_add_u32_e32 v134, s20, v118
	v_add_u32_e32 v136, s34, v119
	v_add_u32_e32 v138, s20, v120
	v_add_u32_e32 v140, s34, v121
	v_add_u32_e32 v142, s20, v122
	v_add_u32_e32 v144, s34, v123
	v_add_u32_e32 v146, s20, v154
	v_add_u32_e32 v148, s34, v155
	v_add_u32_e32 v150, s20, v156
	v_add_u32_e32 v152, s34, v157
	v_ashrrev_i32_e32 v111, 31, v110
	v_lshlrev_b64 v[124:125], 12, v[124:125]
	v_ashrrev_i32_e32 v129, 31, v128
	v_ashrrev_i32_e32 v127, 31, v126
	v_ashrrev_i32_e32 v133, 31, v132
	v_ashrrev_i32_e32 v131, 31, v130
	v_ashrrev_i32_e32 v137, 31, v136
	v_ashrrev_i32_e32 v135, 31, v134
	v_ashrrev_i32_e32 v141, 31, v140
	v_ashrrev_i32_e32 v139, 31, v138
	v_ashrrev_i32_e32 v145, 31, v144
	v_ashrrev_i32_e32 v143, 31, v142
	v_ashrrev_i32_e32 v149, 31, v148
	v_ashrrev_i32_e32 v147, 31, v146
	v_ashrrev_i32_e32 v153, 31, v152
	v_ashrrev_i32_e32 v151, 31, v150
	v_lshlrev_b64 v[110:111], 12, v[110:111]
	v_lshl_add_u64 v[124:125], v[2:3], 0, v[124:125]
	v_lshlrev_b64 v[126:127], 12, v[126:127]
	v_lshlrev_b64 v[128:129], 12, v[128:129]
	v_lshlrev_b64 v[130:131], 12, v[130:131]
	v_lshlrev_b64 v[132:133], 12, v[132:133]
	v_lshlrev_b64 v[134:135], 12, v[134:135]
	v_lshlrev_b64 v[136:137], 12, v[136:137]
	v_lshlrev_b64 v[138:139], 12, v[138:139]
	v_lshlrev_b64 v[140:141], 12, v[140:141]
	v_lshlrev_b64 v[142:143], 12, v[142:143]
	v_lshlrev_b64 v[144:145], 12, v[144:145]
	v_lshlrev_b64 v[146:147], 12, v[146:147]
	v_lshlrev_b64 v[148:149], 12, v[148:149]
	v_lshlrev_b64 v[150:151], 12, v[150:151]
	v_lshlrev_b64 v[152:153], 12, v[152:153]
	v_lshl_add_u64 v[110:111], v[2:3], 0, v[110:111]
	v_lshl_add_u64 v[128:129], v[2:3], 0, v[128:129]
	v_lshl_add_u64 v[126:127], v[2:3], 0, v[126:127]
	v_lshl_add_u64 v[132:133], v[2:3], 0, v[132:133]
	v_lshl_add_u64 v[130:131], v[2:3], 0, v[130:131]
	v_lshl_add_u64 v[136:137], v[2:3], 0, v[136:137]
	v_lshl_add_u64 v[134:135], v[2:3], 0, v[134:135]
	v_lshl_add_u64 v[140:141], v[2:3], 0, v[140:141]
	v_lshl_add_u64 v[138:139], v[2:3], 0, v[138:139]
	v_lshl_add_u64 v[144:145], v[2:3], 0, v[144:145]
	v_lshl_add_u64 v[142:143], v[2:3], 0, v[142:143]
	v_lshl_add_u64 v[148:149], v[2:3], 0, v[148:149]
	v_lshl_add_u64 v[146:147], v[2:3], 0, v[146:147]
	v_lshl_add_u64 v[152:153], v[2:3], 0, v[152:153]
	v_lshl_add_u64 v[150:151], v[2:3], 0, v[150:151]
	global_load_dword v158, v[124:125], off
	global_load_dword v159, v[110:111], off
	global_load_dword v160, v[128:129], off
	global_load_dword v161, v[126:127], off
	global_load_dword v162, v[132:133], off
	global_load_dword v163, v[130:131], off
	global_load_dword v164, v[136:137], off
	global_load_dword v165, v[134:135], off
	global_load_dword v166, v[140:141], off
	global_load_dword v167, v[138:139], off
	global_load_dword v168, v[144:145], off
	global_load_dword v169, v[142:143], off
	global_load_dword v170, v[148:149], off
	global_load_dword v171, v[146:147], off
	global_load_dword v172, v[152:153], off
	global_load_dword v173, v[150:151], off
	s_add_i32 s31, s31, 16
	s_add_i32 s21, s21, 16
	s_add_i32 s35, s35, -16
	v_mad_u64_u32 v[110:111], s[38:39], v113, s43, v[10:11]
	s_cmp_lg_u32 s35, 0
	v_mad_u64_u32 v[124:125], s[38:39], v112, s43, v[10:11]
	v_mad_u64_u32 v[126:127], s[38:39], v115, s43, v[10:11]
	v_mad_u64_u32 v[128:129], s[38:39], v114, s43, v[10:11]
	v_mad_u64_u32 v[130:131], s[38:39], v117, s43, v[10:11]
	v_mad_u64_u32 v[132:133], s[38:39], v116, s43, v[10:11]
	v_mad_u64_u32 v[134:135], s[38:39], v119, s43, v[10:11]
	v_mad_u64_u32 v[136:137], s[38:39], v118, s43, v[10:11]
	v_mad_u64_u32 v[138:139], s[38:39], v121, s43, v[10:11]
	v_mad_u64_u32 v[140:141], s[38:39], v120, s43, v[10:11]
	v_mad_u64_u32 v[142:143], s[38:39], v123, s43, v[10:11]
	v_mad_u64_u32 v[144:145], s[38:39], v122, s43, v[10:11]
	v_mad_u64_u32 v[146:147], s[38:39], v155, s43, v[10:11]
	v_mad_u64_u32 v[148:149], s[38:39], v154, s43, v[10:11]
	v_mad_u64_u32 v[150:151], s[38:39], v157, s43, v[10:11]
	v_mad_u64_u32 v[152:153], s[38:39], v156, s43, v[10:11]
	s_waitcnt vmcnt(31)
	ds_write_b32 v4, v94
	s_waitcnt vmcnt(30)
	ds_write_b32 v56, v95
	s_waitcnt vmcnt(29)
	ds_write_b32 v58, v96
	s_waitcnt vmcnt(28)
	ds_write_b32 v64, v97
	s_waitcnt vmcnt(27)
	ds_write_b32 v66, v98
	s_waitcnt vmcnt(26)
	ds_write_b32 v68, v99
	s_waitcnt vmcnt(25)
	ds_write_b32 v70, v100
	s_waitcnt vmcnt(24)
	ds_write_b32 v72, v101
	s_waitcnt vmcnt(23)
	ds_write_b32 v74, v102
	s_waitcnt vmcnt(22)
	ds_write_b32 v76, v103
	s_waitcnt vmcnt(21)
	ds_write_b32 v78, v104
	s_waitcnt vmcnt(20)
	ds_write_b32 v80, v105
	s_waitcnt vmcnt(19)
	ds_write_b32 v82, v106
	s_waitcnt vmcnt(18)
	ds_write_b32 v84, v107
	s_waitcnt vmcnt(17)
	ds_write_b32 v86, v108
	s_waitcnt vmcnt(16)
	ds_write_b32 v88, v109
	s_waitcnt vmcnt(15)
	ds_write_b32 v110, v158
	s_waitcnt vmcnt(14)
	ds_write_b32 v124, v159
	s_waitcnt vmcnt(13)
	ds_write_b32 v126, v160
	s_waitcnt vmcnt(12)
	ds_write_b32 v128, v161
	s_waitcnt vmcnt(11)
	ds_write_b32 v130, v162
	s_waitcnt vmcnt(10)
	ds_write_b32 v132, v163
	s_waitcnt vmcnt(9)
	ds_write_b32 v134, v164
	s_waitcnt vmcnt(8)
	ds_write_b32 v136, v165
	s_waitcnt vmcnt(7)
	ds_write_b32 v138, v166
	s_waitcnt vmcnt(6)
	ds_write_b32 v140, v167
	s_waitcnt vmcnt(5)
	ds_write_b32 v142, v168
	s_waitcnt vmcnt(4)
	ds_write_b32 v144, v169
	s_waitcnt vmcnt(3)
	ds_write_b32 v146, v170
	s_waitcnt vmcnt(2)
	ds_write_b32 v148, v171
	s_waitcnt vmcnt(1)
	ds_write_b32 v150, v172
	s_waitcnt vmcnt(0)
	ds_write_b32 v152, v173

.LBB0_155:
	s_lshl_b32 s36, s21, 1
	s_lshl_b32 s37, s27, 1
	v_or_b32_e32 v21, s36, v1
	v_or_b32_e32 v31, s37, v6
	s_add_i32 s38, s36, 4
	s_add_i32 s39, s37, 4
	s_add_i32 s40, s36, 8
	s_add_i32 s41, s37, 8
	s_add_i32 s49, s36, 12
	s_add_i32 s50, s37, 12
	s_add_i32 s51, s36, 16
	s_add_i32 s52, s37, 16
	s_add_i32 s53, s36, 20
	s_add_i32 s54, s37, 20
	s_add_i32 s55, s36, 24
	s_add_i32 s56, s37, 24
	s_add_i32 s36, s36, 28
	s_add_i32 s37, s37, 28
	v_add_u32_e32 v56, s30, v31
	v_or_b32_e32 v33, s38, v1
	v_or_b32_e32 v35, s39, v6
	v_or_b32_e32 v37, s40, v1
	v_or_b32_e32 v39, s41, v6
	v_or_b32_e32 v41, s49, v1
	v_or_b32_e32 v43, s50, v6
	v_or_b32_e32 v47, s51, v1
	v_or_b32_e32 v49, s52, v6
	v_or_b32_e32 v51, s53, v1
	v_or_b32_e32 v53, s54, v6
	v_or_b32_e32 v90, s55, v1
	v_or_b32_e32 v91, s56, v6
	v_or_b32_e32 v92, s36, v1
	v_or_b32_e32 v93, s37, v6
	v_add_u32_e32 v4, s20, v21
	v_ashrrev_i32_e32 v57, 31, v56
	v_add_u32_e32 v58, s20, v33
	v_add_u32_e32 v64, s30, v35
	v_add_u32_e32 v66, s20, v37
	v_add_u32_e32 v68, s30, v39
	v_add_u32_e32 v70, s20, v41
	v_add_u32_e32 v72, s30, v43
	v_add_u32_e32 v74, s20, v47
	v_add_u32_e32 v76, s30, v49
	v_add_u32_e32 v78, s20, v51
	v_add_u32_e32 v80, s30, v53
	v_add_u32_e32 v82, s20, v90
	v_add_u32_e32 v84, s30, v91
	v_add_u32_e32 v86, s20, v92
	v_add_u32_e32 v88, s30, v93
	v_ashrrev_i32_e32 v5, 31, v4
	v_lshlrev_b64 v[56:57], 12, v[56:57]
	v_ashrrev_i32_e32 v65, 31, v64
	v_ashrrev_i32_e32 v59, 31, v58
	v_ashrrev_i32_e32 v69, 31, v68
	v_ashrrev_i32_e32 v67, 31, v66
	v_ashrrev_i32_e32 v73, 31, v72
	v_ashrrev_i32_e32 v71, 31, v70
	v_ashrrev_i32_e32 v77, 31, v76
	v_ashrrev_i32_e32 v75, 31, v74
	v_ashrrev_i32_e32 v81, 31, v80
	v_ashrrev_i32_e32 v79, 31, v78
	v_ashrrev_i32_e32 v85, 31, v84
	v_ashrrev_i32_e32 v83, 31, v82
	v_ashrrev_i32_e32 v89, 31, v88
	v_ashrrev_i32_e32 v87, 31, v86
	v_lshlrev_b64 v[4:5], 12, v[4:5]
	v_lshl_add_u64 v[56:57], v[2:3], 0, v[56:57]
	v_lshlrev_b64 v[58:59], 12, v[58:59]
	v_lshlrev_b64 v[64:65], 12, v[64:65]
	v_lshlrev_b64 v[66:67], 12, v[66:67]
	v_lshlrev_b64 v[68:69], 12, v[68:69]
	v_lshlrev_b64 v[70:71], 12, v[70:71]
	v_lshlrev_b64 v[72:73], 12, v[72:73]
	v_lshlrev_b64 v[74:75], 12, v[74:75]
	v_lshlrev_b64 v[76:77], 12, v[76:77]
	v_lshlrev_b64 v[78:79], 12, v[78:79]
	v_lshlrev_b64 v[80:81], 12, v[80:81]
	v_lshlrev_b64 v[82:83], 12, v[82:83]
	v_lshlrev_b64 v[84:85], 12, v[84:85]
	v_lshlrev_b64 v[86:87], 12, v[86:87]
	v_lshlrev_b64 v[88:89], 12, v[88:89]
	v_lshl_add_u64 v[4:5], v[2:3], 0, v[4:5]
	v_lshl_add_u64 v[64:65], v[2:3], 0, v[64:65]
	v_lshl_add_u64 v[58:59], v[2:3], 0, v[58:59]
	v_lshl_add_u64 v[68:69], v[2:3], 0, v[68:69]
	v_lshl_add_u64 v[66:67], v[2:3], 0, v[66:67]
	v_lshl_add_u64 v[72:73], v[2:3], 0, v[72:73]
	v_lshl_add_u64 v[70:71], v[2:3], 0, v[70:71]
	v_lshl_add_u64 v[76:77], v[2:3], 0, v[76:77]
	v_lshl_add_u64 v[74:75], v[2:3], 0, v[74:75]
	v_lshl_add_u64 v[80:81], v[2:3], 0, v[80:81]
	v_lshl_add_u64 v[78:79], v[2:3], 0, v[78:79]
	v_lshl_add_u64 v[84:85], v[2:3], 0, v[84:85]
	v_lshl_add_u64 v[82:83], v[2:3], 0, v[82:83]
	v_lshl_add_u64 v[88:89], v[2:3], 0, v[88:89]
	v_lshl_add_u64 v[86:87], v[2:3], 0, v[86:87]
	global_load_dword v94, v[56:57], off
	global_load_dword v95, v[4:5], off
	global_load_dword v96, v[64:65], off
	global_load_dword v97, v[58:59], off
	global_load_dword v98, v[68:69], off
	global_load_dword v99, v[66:67], off
	global_load_dword v100, v[72:73], off
	global_load_dword v101, v[70:71], off
	global_load_dword v102, v[76:77], off
	global_load_dword v103, v[74:75], off
	global_load_dword v104, v[80:81], off
	global_load_dword v105, v[78:79], off
	global_load_dword v106, v[84:85], off
	global_load_dword v107, v[82:83], off
	global_load_dword v108, v[88:89], off
	global_load_dword v109, v[86:87], off
	s_add_i32 s27, s27, 16
	s_add_i32 s21, s21, 16
	s_add_i32 s31, s31, -16
	v_mad_u64_u32 v[4:5], s[36:37], v31, s43, v[10:11]
	s_cmp_lg_u32 s31, 0
	v_mad_u64_u32 v[56:57], s[36:37], v21, s43, v[10:11]
	v_mad_u64_u32 v[58:59], s[36:37], v35, s43, v[10:11]
	v_mad_u64_u32 v[64:65], s[36:37], v33, s43, v[10:11]
	v_mad_u64_u32 v[66:67], s[36:37], v39, s43, v[10:11]
	v_mad_u64_u32 v[68:69], s[36:37], v37, s43, v[10:11]
	v_mad_u64_u32 v[70:71], s[36:37], v43, s43, v[10:11]
	v_mad_u64_u32 v[72:73], s[36:37], v41, s43, v[10:11]
	v_mad_u64_u32 v[74:75], s[36:37], v49, s43, v[10:11]
	v_mad_u64_u32 v[76:77], s[36:37], v47, s43, v[10:11]
	v_mad_u64_u32 v[78:79], s[36:37], v53, s43, v[10:11]
	v_mad_u64_u32 v[80:81], s[36:37], v51, s43, v[10:11]
	v_mad_u64_u32 v[82:83], s[36:37], v91, s43, v[10:11]
	v_mad_u64_u32 v[84:85], s[36:37], v90, s43, v[10:11]
	v_mad_u64_u32 v[86:87], s[36:37], v93, s43, v[10:11]
	v_mad_u64_u32 v[88:89], s[36:37], v92, s43, v[10:11]
	s_lshl_b32 s36, s21, 1
	s_lshl_b32 s37, s27, 1
	v_or_b32_e32 v112, s36, v1
	v_or_b32_e32 v113, s37, v6
	s_add_i32 s38, s36, 4
	s_add_i32 s39, s37, 4
	s_add_i32 s40, s36, 8
	s_add_i32 s41, s37, 8
	s_add_i32 s49, s36, 12
	s_add_i32 s50, s37, 12
	s_add_i32 s51, s36, 16
	s_add_i32 s52, s37, 16
	s_add_i32 s53, s36, 20
	s_add_i32 s54, s37, 20
	s_add_i32 s55, s36, 24
	s_add_i32 s56, s37, 24
	s_add_i32 s36, s36, 28
	s_add_i32 s37, s37, 28
	v_add_u32_e32 v124, s30, v113
	v_or_b32_e32 v114, s38, v1
	v_or_b32_e32 v115, s39, v6
	v_or_b32_e32 v116, s40, v1
	v_or_b32_e32 v117, s41, v6
	v_or_b32_e32 v118, s49, v1
	v_or_b32_e32 v119, s50, v6
	v_or_b32_e32 v120, s51, v1
	v_or_b32_e32 v121, s52, v6
	v_or_b32_e32 v122, s53, v1
	v_or_b32_e32 v123, s54, v6
	v_or_b32_e32 v154, s55, v1
	v_or_b32_e32 v155, s56, v6
	v_or_b32_e32 v156, s36, v1
	v_or_b32_e32 v157, s37, v6
	v_add_u32_e32 v110, s20, v112
	v_ashrrev_i32_e32 v125, 31, v124
	v_add_u32_e32 v126, s20, v114
	v_add_u32_e32 v128, s30, v115
	v_add_u32_e32 v130, s20, v116
	v_add_u32_e32 v132, s30, v117
	v_add_u32_e32 v134, s20, v118
	v_add_u32_e32 v136, s30, v119
	v_add_u32_e32 v138, s20, v120
	v_add_u32_e32 v140, s30, v121
	v_add_u32_e32 v142, s20, v122
	v_add_u32_e32 v144, s30, v123
	v_add_u32_e32 v146, s20, v154
	v_add_u32_e32 v148, s30, v155
	v_add_u32_e32 v150, s20, v156
	v_add_u32_e32 v152, s30, v157
	v_ashrrev_i32_e32 v111, 31, v110
	v_lshlrev_b64 v[124:125], 12, v[124:125]
	v_ashrrev_i32_e32 v129, 31, v128
	v_ashrrev_i32_e32 v127, 31, v126
	v_ashrrev_i32_e32 v133, 31, v132
	v_ashrrev_i32_e32 v131, 31, v130
	v_ashrrev_i32_e32 v137, 31, v136
	v_ashrrev_i32_e32 v135, 31, v134
	v_ashrrev_i32_e32 v141, 31, v140
	v_ashrrev_i32_e32 v139, 31, v138
	v_ashrrev_i32_e32 v145, 31, v144
	v_ashrrev_i32_e32 v143, 31, v142
	v_ashrrev_i32_e32 v149, 31, v148
	v_ashrrev_i32_e32 v147, 31, v146
	v_ashrrev_i32_e32 v153, 31, v152
	v_ashrrev_i32_e32 v151, 31, v150
	v_lshlrev_b64 v[110:111], 12, v[110:111]
	v_lshl_add_u64 v[124:125], v[2:3], 0, v[124:125]
	v_lshlrev_b64 v[126:127], 12, v[126:127]
	v_lshlrev_b64 v[128:129], 12, v[128:129]
	v_lshlrev_b64 v[130:131], 12, v[130:131]
	v_lshlrev_b64 v[132:133], 12, v[132:133]
	v_lshlrev_b64 v[134:135], 12, v[134:135]
	v_lshlrev_b64 v[136:137], 12, v[136:137]
	v_lshlrev_b64 v[138:139], 12, v[138:139]
	v_lshlrev_b64 v[140:141], 12, v[140:141]
	v_lshlrev_b64 v[142:143], 12, v[142:143]
	v_lshlrev_b64 v[144:145], 12, v[144:145]
	v_lshlrev_b64 v[146:147], 12, v[146:147]
	v_lshlrev_b64 v[148:149], 12, v[148:149]
	v_lshlrev_b64 v[150:151], 12, v[150:151]
	v_lshlrev_b64 v[152:153], 12, v[152:153]
	v_lshl_add_u64 v[110:111], v[2:3], 0, v[110:111]
	v_lshl_add_u64 v[128:129], v[2:3], 0, v[128:129]
	v_lshl_add_u64 v[126:127], v[2:3], 0, v[126:127]
	v_lshl_add_u64 v[132:133], v[2:3], 0, v[132:133]
	v_lshl_add_u64 v[130:131], v[2:3], 0, v[130:131]
	v_lshl_add_u64 v[136:137], v[2:3], 0, v[136:137]
	v_lshl_add_u64 v[134:135], v[2:3], 0, v[134:135]
	v_lshl_add_u64 v[140:141], v[2:3], 0, v[140:141]
	v_lshl_add_u64 v[138:139], v[2:3], 0, v[138:139]
	v_lshl_add_u64 v[144:145], v[2:3], 0, v[144:145]
	v_lshl_add_u64 v[142:143], v[2:3], 0, v[142:143]
	v_lshl_add_u64 v[148:149], v[2:3], 0, v[148:149]
	v_lshl_add_u64 v[146:147], v[2:3], 0, v[146:147]
	v_lshl_add_u64 v[152:153], v[2:3], 0, v[152:153]
	v_lshl_add_u64 v[150:151], v[2:3], 0, v[150:151]
	global_load_dword v158, v[124:125], off
	global_load_dword v159, v[110:111], off
	global_load_dword v160, v[128:129], off
	global_load_dword v161, v[126:127], off
	global_load_dword v162, v[132:133], off
	global_load_dword v163, v[130:131], off
	global_load_dword v164, v[136:137], off
	global_load_dword v165, v[134:135], off
	global_load_dword v166, v[140:141], off
	global_load_dword v167, v[138:139], off
	global_load_dword v168, v[144:145], off
	global_load_dword v169, v[142:143], off
	global_load_dword v170, v[148:149], off
	global_load_dword v171, v[146:147], off
	global_load_dword v172, v[152:153], off
	global_load_dword v173, v[150:151], off
	s_add_i32 s27, s27, 16
	s_add_i32 s21, s21, 16
	s_add_i32 s31, s31, -16
	v_mad_u64_u32 v[110:111], s[36:37], v113, s43, v[10:11]
	s_cmp_lg_u32 s31, 0
	v_mad_u64_u32 v[124:125], s[36:37], v112, s43, v[10:11]
	v_mad_u64_u32 v[126:127], s[36:37], v115, s43, v[10:11]
	v_mad_u64_u32 v[128:129], s[36:37], v114, s43, v[10:11]
	v_mad_u64_u32 v[130:131], s[36:37], v117, s43, v[10:11]
	v_mad_u64_u32 v[132:133], s[36:37], v116, s43, v[10:11]
	v_mad_u64_u32 v[134:135], s[36:37], v119, s43, v[10:11]
	v_mad_u64_u32 v[136:137], s[36:37], v118, s43, v[10:11]
	v_mad_u64_u32 v[138:139], s[36:37], v121, s43, v[10:11]
	v_mad_u64_u32 v[140:141], s[36:37], v120, s43, v[10:11]
	v_mad_u64_u32 v[142:143], s[36:37], v123, s43, v[10:11]
	v_mad_u64_u32 v[144:145], s[36:37], v122, s43, v[10:11]
	v_mad_u64_u32 v[146:147], s[36:37], v155, s43, v[10:11]
	v_mad_u64_u32 v[148:149], s[36:37], v154, s43, v[10:11]
	v_mad_u64_u32 v[150:151], s[36:37], v157, s43, v[10:11]
	v_mad_u64_u32 v[152:153], s[36:37], v156, s43, v[10:11]
	s_waitcnt vmcnt(31)
	ds_write_b32 v4, v94
	s_waitcnt vmcnt(30)
	ds_write_b32 v56, v95
	s_waitcnt vmcnt(29)
	ds_write_b32 v58, v96
	s_waitcnt vmcnt(28)
	ds_write_b32 v64, v97
	s_waitcnt vmcnt(27)
	ds_write_b32 v66, v98
	s_waitcnt vmcnt(26)
	ds_write_b32 v68, v99
	s_waitcnt vmcnt(25)
	ds_write_b32 v70, v100
	s_waitcnt vmcnt(24)
	ds_write_b32 v72, v101
	s_waitcnt vmcnt(23)
	ds_write_b32 v74, v102
	s_waitcnt vmcnt(22)
	ds_write_b32 v76, v103
	s_waitcnt vmcnt(21)
	ds_write_b32 v78, v104
	s_waitcnt vmcnt(20)
	ds_write_b32 v80, v105
	s_waitcnt vmcnt(19)
	ds_write_b32 v82, v106
	s_waitcnt vmcnt(18)
	ds_write_b32 v84, v107
	s_waitcnt vmcnt(17)
	ds_write_b32 v86, v108
	s_waitcnt vmcnt(16)
	ds_write_b32 v88, v109
	s_waitcnt vmcnt(15)
	ds_write_b32 v110, v158
	s_waitcnt vmcnt(14)
	ds_write_b32 v124, v159
	s_waitcnt vmcnt(13)
	ds_write_b32 v126, v160
	s_waitcnt vmcnt(12)
	ds_write_b32 v128, v161
	s_waitcnt vmcnt(11)
	ds_write_b32 v130, v162
	s_waitcnt vmcnt(10)
	ds_write_b32 v132, v163
	s_waitcnt vmcnt(9)
	ds_write_b32 v134, v164
	s_waitcnt vmcnt(8)
	ds_write_b32 v136, v165
	s_waitcnt vmcnt(7)
	ds_write_b32 v138, v166
	s_waitcnt vmcnt(6)
	ds_write_b32 v140, v167
	s_waitcnt vmcnt(5)
	ds_write_b32 v142, v168
	s_waitcnt vmcnt(4)
	ds_write_b32 v144, v169
	s_waitcnt vmcnt(3)
	ds_write_b32 v146, v170
	s_waitcnt vmcnt(2)
	ds_write_b32 v148, v171
	s_waitcnt vmcnt(1)
	ds_write_b32 v150, v172
	s_waitcnt vmcnt(0)
	ds_write_b32 v152, v173

.LBB0_169:
	s_lshl_b32 s31, s21, 1
	s_lshl_b32 s36, s23, 1
	v_or_b32_e32 v21, s31, v1
	v_or_b32_e32 v31, s36, v6
	s_add_i32 s37, s31, 4
	s_add_i32 s38, s36, 4
	s_add_i32 s39, s31, 8
	s_add_i32 s40, s36, 8
	s_add_i32 s41, s31, 12
	s_add_i32 s47, s36, 12
	s_add_i32 s48, s31, 16
	s_add_i32 s49, s36, 16
	s_add_i32 s50, s31, 20
	s_add_i32 s51, s36, 20
	s_add_i32 s52, s31, 24
	s_add_i32 s53, s36, 24
	s_add_i32 s31, s31, 28
	s_add_i32 s36, s36, 28
	v_add_u32_e32 v56, s30, v31
	v_or_b32_e32 v33, s37, v1
	v_or_b32_e32 v35, s38, v6
	v_or_b32_e32 v37, s39, v1
	v_or_b32_e32 v39, s40, v6
	v_or_b32_e32 v41, s41, v1
	v_or_b32_e32 v43, s47, v6
	v_or_b32_e32 v47, s48, v1
	v_or_b32_e32 v49, s49, v6
	v_or_b32_e32 v51, s50, v1
	v_or_b32_e32 v53, s51, v6
	v_or_b32_e32 v90, s52, v1
	v_or_b32_e32 v91, s53, v6
	v_or_b32_e32 v92, s31, v1
	v_or_b32_e32 v93, s36, v6
	v_add_u32_e32 v4, s20, v21
	v_ashrrev_i32_e32 v57, 31, v56
	v_add_u32_e32 v58, s20, v33
	v_add_u32_e32 v64, s30, v35
	v_add_u32_e32 v66, s20, v37
	v_add_u32_e32 v68, s30, v39
	v_add_u32_e32 v70, s20, v41
	v_add_u32_e32 v72, s30, v43
	v_add_u32_e32 v74, s20, v47
	v_add_u32_e32 v76, s30, v49
	v_add_u32_e32 v78, s20, v51
	v_add_u32_e32 v80, s30, v53
	v_add_u32_e32 v82, s20, v90
	v_add_u32_e32 v84, s30, v91
	v_add_u32_e32 v86, s20, v92
	v_add_u32_e32 v88, s30, v93
	v_ashrrev_i32_e32 v5, 31, v4
	v_lshlrev_b64 v[56:57], 12, v[56:57]
	v_ashrrev_i32_e32 v65, 31, v64
	v_ashrrev_i32_e32 v59, 31, v58
	v_ashrrev_i32_e32 v69, 31, v68
	v_ashrrev_i32_e32 v67, 31, v66
	v_ashrrev_i32_e32 v73, 31, v72
	v_ashrrev_i32_e32 v71, 31, v70
	v_ashrrev_i32_e32 v77, 31, v76
	v_ashrrev_i32_e32 v75, 31, v74
	v_ashrrev_i32_e32 v81, 31, v80
	v_ashrrev_i32_e32 v79, 31, v78
	v_ashrrev_i32_e32 v85, 31, v84
	v_ashrrev_i32_e32 v83, 31, v82
	v_ashrrev_i32_e32 v89, 31, v88
	v_ashrrev_i32_e32 v87, 31, v86
	v_lshlrev_b64 v[4:5], 12, v[4:5]
	v_lshl_add_u64 v[56:57], v[2:3], 0, v[56:57]
	v_lshlrev_b64 v[58:59], 12, v[58:59]
	v_lshlrev_b64 v[64:65], 12, v[64:65]
	v_lshlrev_b64 v[66:67], 12, v[66:67]
	v_lshlrev_b64 v[68:69], 12, v[68:69]
	v_lshlrev_b64 v[70:71], 12, v[70:71]
	v_lshlrev_b64 v[72:73], 12, v[72:73]
	v_lshlrev_b64 v[74:75], 12, v[74:75]
	v_lshlrev_b64 v[76:77], 12, v[76:77]
	v_lshlrev_b64 v[78:79], 12, v[78:79]
	v_lshlrev_b64 v[80:81], 12, v[80:81]
	v_lshlrev_b64 v[82:83], 12, v[82:83]
	v_lshlrev_b64 v[84:85], 12, v[84:85]
	v_lshlrev_b64 v[86:87], 12, v[86:87]
	v_lshlrev_b64 v[88:89], 12, v[88:89]
	v_lshl_add_u64 v[4:5], v[2:3], 0, v[4:5]
	v_lshl_add_u64 v[64:65], v[2:3], 0, v[64:65]
	v_lshl_add_u64 v[58:59], v[2:3], 0, v[58:59]
	v_lshl_add_u64 v[68:69], v[2:3], 0, v[68:69]
	v_lshl_add_u64 v[66:67], v[2:3], 0, v[66:67]
	v_lshl_add_u64 v[72:73], v[2:3], 0, v[72:73]
	v_lshl_add_u64 v[70:71], v[2:3], 0, v[70:71]
	v_lshl_add_u64 v[76:77], v[2:3], 0, v[76:77]
	v_lshl_add_u64 v[74:75], v[2:3], 0, v[74:75]
	v_lshl_add_u64 v[80:81], v[2:3], 0, v[80:81]
	v_lshl_add_u64 v[78:79], v[2:3], 0, v[78:79]
	v_lshl_add_u64 v[84:85], v[2:3], 0, v[84:85]
	v_lshl_add_u64 v[82:83], v[2:3], 0, v[82:83]
	v_lshl_add_u64 v[88:89], v[2:3], 0, v[88:89]
	v_lshl_add_u64 v[86:87], v[2:3], 0, v[86:87]
	global_load_dword v94, v[56:57], off
	global_load_dword v95, v[4:5], off
	global_load_dword v96, v[64:65], off
	global_load_dword v97, v[58:59], off
	global_load_dword v98, v[68:69], off
	global_load_dword v99, v[66:67], off
	global_load_dword v100, v[72:73], off
	global_load_dword v101, v[70:71], off
	global_load_dword v102, v[76:77], off
	global_load_dword v103, v[74:75], off
	global_load_dword v104, v[80:81], off
	global_load_dword v105, v[78:79], off
	global_load_dword v106, v[84:85], off
	global_load_dword v107, v[82:83], off
	global_load_dword v108, v[88:89], off
	global_load_dword v109, v[86:87], off
	s_add_i32 s23, s23, 16
	s_add_i32 s21, s21, 16
	s_add_i32 s27, s27, -16
	v_mad_u64_u32 v[4:5], s[36:37], v31, s43, v[10:11]
	s_cmp_lg_u32 s27, 0
	v_mad_u64_u32 v[56:57], s[36:37], v21, s43, v[10:11]
	v_mad_u64_u32 v[58:59], s[36:37], v35, s43, v[10:11]
	v_mad_u64_u32 v[64:65], s[36:37], v33, s43, v[10:11]
	v_mad_u64_u32 v[66:67], s[36:37], v39, s43, v[10:11]
	v_mad_u64_u32 v[68:69], s[36:37], v37, s43, v[10:11]
	v_mad_u64_u32 v[70:71], s[36:37], v43, s43, v[10:11]
	v_mad_u64_u32 v[72:73], s[36:37], v41, s43, v[10:11]
	v_mad_u64_u32 v[74:75], s[36:37], v49, s43, v[10:11]
	v_mad_u64_u32 v[76:77], s[36:37], v47, s43, v[10:11]
	v_mad_u64_u32 v[78:79], s[36:37], v53, s43, v[10:11]
	v_mad_u64_u32 v[80:81], s[36:37], v51, s43, v[10:11]
	v_mad_u64_u32 v[82:83], s[36:37], v91, s43, v[10:11]
	v_mad_u64_u32 v[84:85], s[36:37], v90, s43, v[10:11]
	v_mad_u64_u32 v[86:87], s[36:37], v93, s43, v[10:11]
	v_mad_u64_u32 v[88:89], s[36:37], v92, s43, v[10:11]
	s_lshl_b32 s31, s21, 1
	s_lshl_b32 s36, s23, 1
	v_or_b32_e32 v112, s31, v1
	v_or_b32_e32 v113, s36, v6
	s_add_i32 s37, s31, 4
	s_add_i32 s38, s36, 4
	s_add_i32 s39, s31, 8
	s_add_i32 s40, s36, 8
	s_add_i32 s41, s31, 12
	s_add_i32 s47, s36, 12
	s_add_i32 s48, s31, 16
	s_add_i32 s49, s36, 16
	s_add_i32 s50, s31, 20
	s_add_i32 s51, s36, 20
	s_add_i32 s52, s31, 24
	s_add_i32 s53, s36, 24
	s_add_i32 s31, s31, 28
	s_add_i32 s36, s36, 28
	v_add_u32_e32 v124, s30, v113
	v_or_b32_e32 v114, s37, v1
	v_or_b32_e32 v115, s38, v6
	v_or_b32_e32 v116, s39, v1
	v_or_b32_e32 v117, s40, v6
	v_or_b32_e32 v118, s41, v1
	v_or_b32_e32 v119, s47, v6
	v_or_b32_e32 v120, s48, v1
	v_or_b32_e32 v121, s49, v6
	v_or_b32_e32 v122, s50, v1
	v_or_b32_e32 v123, s51, v6
	v_or_b32_e32 v154, s52, v1
	v_or_b32_e32 v155, s53, v6
	v_or_b32_e32 v156, s31, v1
	v_or_b32_e32 v157, s36, v6
	v_add_u32_e32 v110, s20, v112
	v_ashrrev_i32_e32 v125, 31, v124
	v_add_u32_e32 v126, s20, v114
	v_add_u32_e32 v128, s30, v115
	v_add_u32_e32 v130, s20, v116
	v_add_u32_e32 v132, s30, v117
	v_add_u32_e32 v134, s20, v118
	v_add_u32_e32 v136, s30, v119
	v_add_u32_e32 v138, s20, v120
	v_add_u32_e32 v140, s30, v121
	v_add_u32_e32 v142, s20, v122
	v_add_u32_e32 v144, s30, v123
	v_add_u32_e32 v146, s20, v154
	v_add_u32_e32 v148, s30, v155
	v_add_u32_e32 v150, s20, v156
	v_add_u32_e32 v152, s30, v157
	v_ashrrev_i32_e32 v111, 31, v110
	v_lshlrev_b64 v[124:125], 12, v[124:125]
	v_ashrrev_i32_e32 v129, 31, v128
	v_ashrrev_i32_e32 v127, 31, v126
	v_ashrrev_i32_e32 v133, 31, v132
	v_ashrrev_i32_e32 v131, 31, v130
	v_ashrrev_i32_e32 v137, 31, v136
	v_ashrrev_i32_e32 v135, 31, v134
	v_ashrrev_i32_e32 v141, 31, v140
	v_ashrrev_i32_e32 v139, 31, v138
	v_ashrrev_i32_e32 v145, 31, v144
	v_ashrrev_i32_e32 v143, 31, v142
	v_ashrrev_i32_e32 v149, 31, v148
	v_ashrrev_i32_e32 v147, 31, v146
	v_ashrrev_i32_e32 v153, 31, v152
	v_ashrrev_i32_e32 v151, 31, v150
	v_lshlrev_b64 v[110:111], 12, v[110:111]
	v_lshl_add_u64 v[124:125], v[2:3], 0, v[124:125]
	v_lshlrev_b64 v[126:127], 12, v[126:127]
	v_lshlrev_b64 v[128:129], 12, v[128:129]
	v_lshlrev_b64 v[130:131], 12, v[130:131]
	v_lshlrev_b64 v[132:133], 12, v[132:133]
	v_lshlrev_b64 v[134:135], 12, v[134:135]
	v_lshlrev_b64 v[136:137], 12, v[136:137]
	v_lshlrev_b64 v[138:139], 12, v[138:139]
	v_lshlrev_b64 v[140:141], 12, v[140:141]
	v_lshlrev_b64 v[142:143], 12, v[142:143]
	v_lshlrev_b64 v[144:145], 12, v[144:145]
	v_lshlrev_b64 v[146:147], 12, v[146:147]
	v_lshlrev_b64 v[148:149], 12, v[148:149]
	v_lshlrev_b64 v[150:151], 12, v[150:151]
	v_lshlrev_b64 v[152:153], 12, v[152:153]
	v_lshl_add_u64 v[110:111], v[2:3], 0, v[110:111]
	v_lshl_add_u64 v[128:129], v[2:3], 0, v[128:129]
	v_lshl_add_u64 v[126:127], v[2:3], 0, v[126:127]
	v_lshl_add_u64 v[132:133], v[2:3], 0, v[132:133]
	v_lshl_add_u64 v[130:131], v[2:3], 0, v[130:131]
	v_lshl_add_u64 v[136:137], v[2:3], 0, v[136:137]
	v_lshl_add_u64 v[134:135], v[2:3], 0, v[134:135]
	v_lshl_add_u64 v[140:141], v[2:3], 0, v[140:141]
	v_lshl_add_u64 v[138:139], v[2:3], 0, v[138:139]
	v_lshl_add_u64 v[144:145], v[2:3], 0, v[144:145]
	v_lshl_add_u64 v[142:143], v[2:3], 0, v[142:143]
	v_lshl_add_u64 v[148:149], v[2:3], 0, v[148:149]
	v_lshl_add_u64 v[146:147], v[2:3], 0, v[146:147]
	v_lshl_add_u64 v[152:153], v[2:3], 0, v[152:153]
	v_lshl_add_u64 v[150:151], v[2:3], 0, v[150:151]
	global_load_dword v158, v[124:125], off
	global_load_dword v159, v[110:111], off
	global_load_dword v160, v[128:129], off
	global_load_dword v161, v[126:127], off
	global_load_dword v162, v[132:133], off
	global_load_dword v163, v[130:131], off
	global_load_dword v164, v[136:137], off
	global_load_dword v165, v[134:135], off
	global_load_dword v166, v[140:141], off
	global_load_dword v167, v[138:139], off
	global_load_dword v168, v[144:145], off
	global_load_dword v169, v[142:143], off
	global_load_dword v170, v[148:149], off
	global_load_dword v171, v[146:147], off
	global_load_dword v172, v[152:153], off
	global_load_dword v173, v[150:151], off
	s_add_i32 s23, s23, 16
	s_add_i32 s21, s21, 16
	s_add_i32 s27, s27, -16
	v_mad_u64_u32 v[110:111], s[36:37], v113, s43, v[10:11]
	s_cmp_lg_u32 s27, 0
	v_mad_u64_u32 v[124:125], s[36:37], v112, s43, v[10:11]
	v_mad_u64_u32 v[126:127], s[36:37], v115, s43, v[10:11]
	v_mad_u64_u32 v[128:129], s[36:37], v114, s43, v[10:11]
	v_mad_u64_u32 v[130:131], s[36:37], v117, s43, v[10:11]
	v_mad_u64_u32 v[132:133], s[36:37], v116, s43, v[10:11]
	v_mad_u64_u32 v[134:135], s[36:37], v119, s43, v[10:11]
	v_mad_u64_u32 v[136:137], s[36:37], v118, s43, v[10:11]
	v_mad_u64_u32 v[138:139], s[36:37], v121, s43, v[10:11]
	v_mad_u64_u32 v[140:141], s[36:37], v120, s43, v[10:11]
	v_mad_u64_u32 v[142:143], s[36:37], v123, s43, v[10:11]
	v_mad_u64_u32 v[144:145], s[36:37], v122, s43, v[10:11]
	v_mad_u64_u32 v[146:147], s[36:37], v155, s43, v[10:11]
	v_mad_u64_u32 v[148:149], s[36:37], v154, s43, v[10:11]
	v_mad_u64_u32 v[150:151], s[36:37], v157, s43, v[10:11]
	v_mad_u64_u32 v[152:153], s[36:37], v156, s43, v[10:11]
	s_waitcnt vmcnt(31)
	ds_write_b32 v4, v94
	s_waitcnt vmcnt(30)
	ds_write_b32 v56, v95
	s_waitcnt vmcnt(29)
	ds_write_b32 v58, v96
	s_waitcnt vmcnt(28)
	ds_write_b32 v64, v97
	s_waitcnt vmcnt(27)
	ds_write_b32 v66, v98
	s_waitcnt vmcnt(26)
	ds_write_b32 v68, v99
	s_waitcnt vmcnt(25)
	ds_write_b32 v70, v100
	s_waitcnt vmcnt(24)
	ds_write_b32 v72, v101
	s_waitcnt vmcnt(23)
	ds_write_b32 v74, v102
	s_waitcnt vmcnt(22)
	ds_write_b32 v76, v103
	s_waitcnt vmcnt(21)
	ds_write_b32 v78, v104
	s_waitcnt vmcnt(20)
	ds_write_b32 v80, v105
	s_waitcnt vmcnt(19)
	ds_write_b32 v82, v106
	s_waitcnt vmcnt(18)
	ds_write_b32 v84, v107
	s_waitcnt vmcnt(17)
	ds_write_b32 v86, v108
	s_waitcnt vmcnt(16)
	ds_write_b32 v88, v109
	s_waitcnt vmcnt(15)
	ds_write_b32 v110, v158
	s_waitcnt vmcnt(14)
	ds_write_b32 v124, v159
	s_waitcnt vmcnt(13)
	ds_write_b32 v126, v160
	s_waitcnt vmcnt(12)
	ds_write_b32 v128, v161
	s_waitcnt vmcnt(11)
	ds_write_b32 v130, v162
	s_waitcnt vmcnt(10)
	ds_write_b32 v132, v163
	s_waitcnt vmcnt(9)
	ds_write_b32 v134, v164
	s_waitcnt vmcnt(8)
	ds_write_b32 v136, v165
	s_waitcnt vmcnt(7)
	ds_write_b32 v138, v166
	s_waitcnt vmcnt(6)
	ds_write_b32 v140, v167
	s_waitcnt vmcnt(5)
	ds_write_b32 v142, v168
	s_waitcnt vmcnt(4)
	ds_write_b32 v144, v169
	s_waitcnt vmcnt(3)
	ds_write_b32 v146, v170
	s_waitcnt vmcnt(2)
	ds_write_b32 v148, v171
	s_waitcnt vmcnt(1)
	ds_write_b32 v150, v172
	s_waitcnt vmcnt(0)
	ds_write_b32 v152, v173

.LBB0_185:
	s_lshl_b32 s41, s27, 1
	s_lshl_b32 s42, s20, 1
	v_or_b32_e32 v25, s41, v1
	v_or_b32_e32 v27, s42, v6
	s_add_i32 s43, s41, 4
	s_add_i32 s44, s42, 4
	s_add_i32 s45, s41, 8
	s_add_i32 s46, s42, 8
	s_add_i32 s47, s41, 12
	s_add_i32 s48, s42, 12
	s_add_i32 s49, s41, 16
	s_add_i32 s50, s42, 16
	s_add_i32 s51, s41, 20
	s_add_i32 s52, s42, 20
	s_add_i32 s53, s41, 24
	s_add_i32 s54, s42, 24
	s_add_i32 s41, s41, 28
	s_add_i32 s42, s42, 28
	v_add_u32_e32 v29, s21, v25
	v_add_u32_e32 v4, s26, v27
	v_or_b32_e32 v64, s43, v1
	v_or_b32_e32 v65, s44, v6
	v_or_b32_e32 v66, s45, v1
	v_or_b32_e32 v67, s46, v6
	v_or_b32_e32 v68, s47, v1
	v_or_b32_e32 v69, s48, v6
	v_or_b32_e32 v70, s49, v1
	v_or_b32_e32 v71, s50, v6
	v_or_b32_e32 v72, s51, v1
	v_or_b32_e32 v73, s52, v6
	v_or_b32_e32 v74, s53, v1
	v_or_b32_e32 v75, s54, v6
	v_or_b32_e32 v76, s41, v1
	v_or_b32_e32 v77, s42, v6
	v_mad_i64_i32 v[4:5], s[42:43], v4, s36, v[2:3]
	v_mad_i64_i32 v[30:31], s[42:43], v29, s36, v[2:3]
	v_add_u32_e32 v29, s21, v64
	v_add_u32_e32 v32, s26, v65
	v_add_u32_e32 v42, s21, v66
	v_add_u32_e32 v40, s26, v67
	v_add_u32_e32 v46, s21, v68
	v_add_u32_e32 v44, s26, v69
	v_add_u32_e32 v50, s21, v70
	v_add_u32_e32 v48, s26, v71
	v_add_u32_e32 v54, s21, v72
	v_add_u32_e32 v52, s26, v73
	v_add_u32_e32 v58, s21, v74
	v_add_u32_e32 v56, s26, v75
	v_add_u32_e32 v62, s21, v76
	v_add_u32_e32 v60, s26, v77
	v_mad_i64_i32 v[32:33], s[42:43], v32, s36, v[2:3]
	v_mad_i64_i32 v[34:35], s[42:43], v29, s36, v[2:3]
	v_mad_i64_i32 v[40:41], s[42:43], v40, s36, v[2:3]
	v_mad_i64_i32 v[42:43], s[42:43], v42, s36, v[2:3]
	v_mad_i64_i32 v[44:45], s[42:43], v44, s36, v[2:3]
	v_mad_i64_i32 v[46:47], s[42:43], v46, s36, v[2:3]
	v_mad_i64_i32 v[48:49], s[42:43], v48, s36, v[2:3]
	v_mad_i64_i32 v[50:51], s[42:43], v50, s36, v[2:3]
	v_mad_i64_i32 v[52:53], s[42:43], v52, s36, v[2:3]
	v_mad_i64_i32 v[54:55], s[42:43], v54, s36, v[2:3]
	v_mad_i64_i32 v[56:57], s[42:43], v56, s36, v[2:3]
	v_mad_i64_i32 v[58:59], s[42:43], v58, s36, v[2:3]
	v_mad_i64_i32 v[60:61], s[42:43], v60, s36, v[2:3]
	v_mad_i64_i32 v[62:63], s[42:43], v62, s36, v[2:3]
	global_load_dword v29, v[4:5], off
	global_load_dword v78, v[30:31], off
	global_load_dword v79, v[32:33], off
	global_load_dword v80, v[34:35], off
	global_load_dword v81, v[40:41], off
	global_load_dword v82, v[42:43], off
	global_load_dword v83, v[44:45], off
	global_load_dword v84, v[46:47], off
	global_load_dword v85, v[48:49], off
	global_load_dword v86, v[50:51], off
	global_load_dword v87, v[52:53], off
	global_load_dword v88, v[54:55], off
	global_load_dword v89, v[56:57], off
	global_load_dword v90, v[58:59], off
	global_load_dword v91, v[60:61], off
	global_load_dword v92, v[62:63], off
	s_add_i32 s20, s20, 16
	s_add_i32 s27, s27, 16
	s_add_i32 s31, s31, -16
	v_mad_u64_u32 v[4:5], s[42:43], v27, s37, v[10:11]
	s_cmp_lg_u32 s31, 0
	v_mad_u64_u32 v[30:31], s[42:43], v25, s37, v[10:11]
	v_mad_u64_u32 v[32:33], s[42:43], v65, s37, v[10:11]
	v_mad_u64_u32 v[34:35], s[42:43], v64, s37, v[10:11]
	v_mad_u64_u32 v[40:41], s[42:43], v67, s37, v[10:11]
	v_mad_u64_u32 v[42:43], s[42:43], v66, s37, v[10:11]
	v_mad_u64_u32 v[44:45], s[42:43], v69, s37, v[10:11]
	v_mad_u64_u32 v[46:47], s[42:43], v68, s37, v[10:11]
	v_mad_u64_u32 v[48:49], s[42:43], v71, s37, v[10:11]
	v_mad_u64_u32 v[50:51], s[42:43], v70, s37, v[10:11]
	v_mad_u64_u32 v[52:53], s[42:43], v73, s37, v[10:11]
	v_mad_u64_u32 v[54:55], s[42:43], v72, s37, v[10:11]
	v_mad_u64_u32 v[56:57], s[42:43], v75, s37, v[10:11]
	v_mad_u64_u32 v[58:59], s[42:43], v74, s37, v[10:11]
	v_mad_u64_u32 v[60:61], s[42:43], v77, s37, v[10:11]
	v_mad_u64_u32 v[62:63], s[42:43], v76, s37, v[10:11]
	s_lshl_b32 s41, s27, 1
	s_lshl_b32 s42, s20, 1
	v_or_b32_e32 v112, s41, v1
	v_or_b32_e32 v113, s42, v6
	s_add_i32 s43, s41, 4
	s_add_i32 s44, s42, 4
	s_add_i32 s45, s41, 8
	s_add_i32 s46, s42, 8
	s_add_i32 s47, s41, 12
	s_add_i32 s48, s42, 12
	s_add_i32 s49, s41, 16
	s_add_i32 s50, s42, 16
	s_add_i32 s51, s41, 20
	s_add_i32 s52, s42, 20
	s_add_i32 s53, s41, 24
	s_add_i32 s54, s42, 24
	s_add_i32 s41, s41, 28
	s_add_i32 s42, s42, 28
	v_add_u32_e32 v114, s21, v112
	v_add_u32_e32 v110, s26, v113
	v_or_b32_e32 v146, s43, v1
	v_or_b32_e32 v147, s44, v6
	v_or_b32_e32 v148, s45, v1
	v_or_b32_e32 v149, s46, v6
	v_or_b32_e32 v150, s47, v1
	v_or_b32_e32 v151, s48, v6
	v_or_b32_e32 v152, s49, v1
	v_or_b32_e32 v153, s50, v6
	v_or_b32_e32 v154, s51, v1
	v_or_b32_e32 v155, s52, v6
	v_or_b32_e32 v156, s53, v1
	v_or_b32_e32 v157, s54, v6
	v_or_b32_e32 v158, s41, v1
	v_or_b32_e32 v159, s42, v6
	v_mad_i64_i32 v[110:111], s[42:43], v110, s36, v[2:3]
	v_mad_i64_i32 v[116:117], s[42:43], v114, s36, v[2:3]
	v_add_u32_e32 v114, s21, v146
	v_add_u32_e32 v118, s26, v147
	v_add_u32_e32 v124, s21, v148
	v_add_u32_e32 v122, s26, v149
	v_add_u32_e32 v128, s21, v150
	v_add_u32_e32 v126, s26, v151
	v_add_u32_e32 v132, s21, v152
	v_add_u32_e32 v130, s26, v153
	v_add_u32_e32 v136, s21, v154
	v_add_u32_e32 v134, s26, v155
	v_add_u32_e32 v140, s21, v156
	v_add_u32_e32 v138, s26, v157
	v_add_u32_e32 v144, s21, v158
	v_add_u32_e32 v142, s26, v159
	v_mad_i64_i32 v[118:119], s[42:43], v118, s36, v[2:3]
	v_mad_i64_i32 v[120:121], s[42:43], v114, s36, v[2:3]
	v_mad_i64_i32 v[122:123], s[42:43], v122, s36, v[2:3]
	v_mad_i64_i32 v[124:125], s[42:43], v124, s36, v[2:3]
	v_mad_i64_i32 v[126:127], s[42:43], v126, s36, v[2:3]
	v_mad_i64_i32 v[128:129], s[42:43], v128, s36, v[2:3]
	v_mad_i64_i32 v[130:131], s[42:43], v130, s36, v[2:3]
	v_mad_i64_i32 v[132:133], s[42:43], v132, s36, v[2:3]
	v_mad_i64_i32 v[134:135], s[42:43], v134, s36, v[2:3]
	v_mad_i64_i32 v[136:137], s[42:43], v136, s36, v[2:3]
	v_mad_i64_i32 v[138:139], s[42:43], v138, s36, v[2:3]
	v_mad_i64_i32 v[140:141], s[42:43], v140, s36, v[2:3]
	v_mad_i64_i32 v[142:143], s[42:43], v142, s36, v[2:3]
	v_mad_i64_i32 v[144:145], s[42:43], v144, s36, v[2:3]
	global_load_dword v114, v[110:111], off
	global_load_dword v160, v[116:117], off
	global_load_dword v161, v[118:119], off
	global_load_dword v162, v[120:121], off
	global_load_dword v163, v[122:123], off
	global_load_dword v164, v[124:125], off
	global_load_dword v165, v[126:127], off
	global_load_dword v166, v[128:129], off
	global_load_dword v167, v[130:131], off
	global_load_dword v168, v[132:133], off
	global_load_dword v169, v[134:135], off
	global_load_dword v170, v[136:137], off
	global_load_dword v171, v[138:139], off
	global_load_dword v172, v[140:141], off
	global_load_dword v173, v[142:143], off
	global_load_dword v174, v[144:145], off
	s_add_i32 s20, s20, 16
	s_add_i32 s27, s27, 16
	s_add_i32 s31, s31, -16
	v_mad_u64_u32 v[110:111], s[42:43], v113, s37, v[10:11]
	s_cmp_lg_u32 s31, 0
	v_mad_u64_u32 v[116:117], s[42:43], v112, s37, v[10:11]
	v_mad_u64_u32 v[118:119], s[42:43], v147, s37, v[10:11]
	v_mad_u64_u32 v[120:121], s[42:43], v146, s37, v[10:11]
	v_mad_u64_u32 v[122:123], s[42:43], v149, s37, v[10:11]
	v_mad_u64_u32 v[124:125], s[42:43], v148, s37, v[10:11]
	v_mad_u64_u32 v[126:127], s[42:43], v151, s37, v[10:11]
	v_mad_u64_u32 v[128:129], s[42:43], v150, s37, v[10:11]
	v_mad_u64_u32 v[130:131], s[42:43], v153, s37, v[10:11]
	v_mad_u64_u32 v[132:133], s[42:43], v152, s37, v[10:11]
	v_mad_u64_u32 v[134:135], s[42:43], v155, s37, v[10:11]
	v_mad_u64_u32 v[136:137], s[42:43], v154, s37, v[10:11]
	v_mad_u64_u32 v[138:139], s[42:43], v157, s37, v[10:11]
	v_mad_u64_u32 v[140:141], s[42:43], v156, s37, v[10:11]
	v_mad_u64_u32 v[142:143], s[42:43], v159, s37, v[10:11]
	v_mad_u64_u32 v[144:145], s[42:43], v158, s37, v[10:11]
	s_waitcnt vmcnt(31)
	ds_write_b32 v4, v29
	s_waitcnt vmcnt(30)
	ds_write_b32 v30, v78
	s_waitcnt vmcnt(29)
	ds_write_b32 v32, v79
	s_waitcnt vmcnt(28)
	ds_write_b32 v34, v80
	s_waitcnt vmcnt(27)
	ds_write_b32 v40, v81
	s_waitcnt vmcnt(26)
	ds_write_b32 v42, v82
	s_waitcnt vmcnt(25)
	ds_write_b32 v44, v83
	s_waitcnt vmcnt(24)
	ds_write_b32 v46, v84
	s_waitcnt vmcnt(23)
	ds_write_b32 v48, v85
	s_waitcnt vmcnt(22)
	ds_write_b32 v50, v86
	s_waitcnt vmcnt(21)
	ds_write_b32 v52, v87
	s_waitcnt vmcnt(20)
	ds_write_b32 v54, v88
	s_waitcnt vmcnt(19)
	ds_write_b32 v56, v89
	s_waitcnt vmcnt(18)
	ds_write_b32 v58, v90
	s_waitcnt vmcnt(17)
	ds_write_b32 v60, v91
	s_waitcnt vmcnt(16)
	ds_write_b32 v62, v92
	s_waitcnt vmcnt(15)
	ds_write_b32 v110, v114
	s_waitcnt vmcnt(14)
	ds_write_b32 v116, v160
	s_waitcnt vmcnt(13)
	ds_write_b32 v118, v161
	s_waitcnt vmcnt(12)
	ds_write_b32 v120, v162
	s_waitcnt vmcnt(11)
	ds_write_b32 v122, v163
	s_waitcnt vmcnt(10)
	ds_write_b32 v124, v164
	s_waitcnt vmcnt(9)
	ds_write_b32 v126, v165
	s_waitcnt vmcnt(8)
	ds_write_b32 v128, v166
	s_waitcnt vmcnt(7)
	ds_write_b32 v130, v167
	s_waitcnt vmcnt(6)
	ds_write_b32 v132, v168
	s_waitcnt vmcnt(5)
	ds_write_b32 v134, v169
	s_waitcnt vmcnt(4)
	ds_write_b32 v136, v170
	s_waitcnt vmcnt(3)
	ds_write_b32 v138, v171
	s_waitcnt vmcnt(2)
	ds_write_b32 v140, v172
	s_waitcnt vmcnt(1)
	ds_write_b32 v142, v173
	s_waitcnt vmcnt(0)
	ds_write_b32 v144, v174

.LBB0_199:
	s_lshl_b32 s38, s21, 1
	s_lshl_b32 s39, s25, 1
	v_or_b32_e32 v25, s38, v1
	v_or_b32_e32 v27, s39, v6
	s_add_i32 s40, s38, 4
	s_add_i32 s41, s39, 4
	s_add_i32 s42, s38, 8
	s_add_i32 s43, s39, 8
	s_add_i32 s44, s38, 12
	s_add_i32 s45, s39, 12
	s_add_i32 s46, s38, 16
	s_add_i32 s47, s39, 16
	s_add_i32 s48, s38, 20
	s_add_i32 s49, s39, 20
	s_add_i32 s50, s38, 24
	s_add_i32 s51, s39, 24
	s_add_i32 s38, s38, 28
	s_add_i32 s39, s39, 28
	v_add_u32_e32 v32, s24, v27
	v_or_b32_e32 v29, s40, v1
	v_or_b32_e32 v66, s41, v6
	v_or_b32_e32 v67, s42, v1
	v_or_b32_e32 v68, s43, v6
	v_or_b32_e32 v69, s44, v1
	v_or_b32_e32 v70, s45, v6
	v_or_b32_e32 v71, s46, v1
	v_or_b32_e32 v72, s47, v6
	v_or_b32_e32 v73, s48, v1
	v_or_b32_e32 v74, s49, v6
	v_or_b32_e32 v75, s50, v1
	v_or_b32_e32 v76, s51, v6
	v_or_b32_e32 v77, s38, v1
	v_or_b32_e32 v78, s39, v6
	v_add_u32_e32 v4, s20, v25
	v_ashrrev_i32_e32 v33, 31, v32
	v_add_u32_e32 v34, s20, v29
	v_add_u32_e32 v40, s24, v66
	v_add_u32_e32 v42, s20, v67
	v_add_u32_e32 v44, s24, v68
	v_add_u32_e32 v46, s20, v69
	v_add_u32_e32 v48, s24, v70
	v_add_u32_e32 v50, s20, v71
	v_add_u32_e32 v52, s24, v72
	v_add_u32_e32 v54, s20, v73
	v_add_u32_e32 v56, s24, v74
	v_add_u32_e32 v58, s20, v75
	v_add_u32_e32 v60, s24, v76
	v_add_u32_e32 v62, s20, v77
	v_add_u32_e32 v64, s24, v78
	v_ashrrev_i32_e32 v5, 31, v4
	v_lshlrev_b64 v[32:33], 12, v[32:33]
	v_ashrrev_i32_e32 v41, 31, v40
	v_ashrrev_i32_e32 v35, 31, v34
	v_ashrrev_i32_e32 v45, 31, v44
	v_ashrrev_i32_e32 v43, 31, v42
	v_ashrrev_i32_e32 v49, 31, v48
	v_ashrrev_i32_e32 v47, 31, v46
	v_ashrrev_i32_e32 v53, 31, v52
	v_ashrrev_i32_e32 v51, 31, v50
	v_ashrrev_i32_e32 v57, 31, v56
	v_ashrrev_i32_e32 v55, 31, v54
	v_ashrrev_i32_e32 v61, 31, v60
	v_ashrrev_i32_e32 v59, 31, v58
	v_ashrrev_i32_e32 v65, 31, v64
	v_ashrrev_i32_e32 v63, 31, v62
	v_lshlrev_b64 v[4:5], 12, v[4:5]
	v_lshl_add_u64 v[32:33], v[2:3], 0, v[32:33]
	v_lshlrev_b64 v[34:35], 12, v[34:35]
	v_lshlrev_b64 v[40:41], 12, v[40:41]
	v_lshlrev_b64 v[42:43], 12, v[42:43]
	v_lshlrev_b64 v[44:45], 12, v[44:45]
	v_lshlrev_b64 v[46:47], 12, v[46:47]
	v_lshlrev_b64 v[48:49], 12, v[48:49]
	v_lshlrev_b64 v[50:51], 12, v[50:51]
	v_lshlrev_b64 v[52:53], 12, v[52:53]
	v_lshlrev_b64 v[54:55], 12, v[54:55]
	v_lshlrev_b64 v[56:57], 12, v[56:57]
	v_lshlrev_b64 v[58:59], 12, v[58:59]
	v_lshlrev_b64 v[60:61], 12, v[60:61]
	v_lshlrev_b64 v[62:63], 12, v[62:63]
	v_lshlrev_b64 v[64:65], 12, v[64:65]
	v_lshl_add_u64 v[4:5], v[2:3], 0, v[4:5]
	v_lshl_add_u64 v[40:41], v[2:3], 0, v[40:41]
	v_lshl_add_u64 v[34:35], v[2:3], 0, v[34:35]
	v_lshl_add_u64 v[44:45], v[2:3], 0, v[44:45]
	v_lshl_add_u64 v[42:43], v[2:3], 0, v[42:43]
	v_lshl_add_u64 v[48:49], v[2:3], 0, v[48:49]
	v_lshl_add_u64 v[46:47], v[2:3], 0, v[46:47]
	v_lshl_add_u64 v[52:53], v[2:3], 0, v[52:53]
	v_lshl_add_u64 v[50:51], v[2:3], 0, v[50:51]
	v_lshl_add_u64 v[56:57], v[2:3], 0, v[56:57]
	v_lshl_add_u64 v[54:55], v[2:3], 0, v[54:55]
	v_lshl_add_u64 v[60:61], v[2:3], 0, v[60:61]
	v_lshl_add_u64 v[58:59], v[2:3], 0, v[58:59]
	v_lshl_add_u64 v[64:65], v[2:3], 0, v[64:65]
	v_lshl_add_u64 v[62:63], v[2:3], 0, v[62:63]
	global_load_dword v79, v[32:33], off
	global_load_dword v80, v[4:5], off
	global_load_dword v81, v[40:41], off
	global_load_dword v82, v[34:35], off
	global_load_dword v83, v[44:45], off
	global_load_dword v84, v[42:43], off
	global_load_dword v85, v[48:49], off
	global_load_dword v86, v[46:47], off
	global_load_dword v87, v[52:53], off
	global_load_dword v88, v[50:51], off
	global_load_dword v89, v[56:57], off
	global_load_dword v90, v[54:55], off
	global_load_dword v91, v[60:61], off
	global_load_dword v92, v[58:59], off
	global_load_dword v93, v[64:65], off
	global_load_dword v94, v[62:63], off
	s_add_i32 s25, s25, 16
	s_add_i32 s21, s21, 16
	s_add_i32 s31, s31, -16
	v_mad_u64_u32 v[4:5], s[38:39], v27, s37, v[10:11]
	s_cmp_lg_u32 s31, 0
	v_mad_u64_u32 v[32:33], s[38:39], v25, s37, v[10:11]
	v_mad_u64_u32 v[34:35], s[38:39], v66, s37, v[10:11]
	v_mad_u64_u32 v[40:41], s[38:39], v29, s37, v[10:11]
	v_mad_u64_u32 v[42:43], s[38:39], v68, s37, v[10:11]
	v_mad_u64_u32 v[44:45], s[38:39], v67, s37, v[10:11]
	v_mad_u64_u32 v[46:47], s[38:39], v70, s37, v[10:11]
	v_mad_u64_u32 v[48:49], s[38:39], v69, s37, v[10:11]
	v_mad_u64_u32 v[50:51], s[38:39], v72, s37, v[10:11]
	v_mad_u64_u32 v[52:53], s[38:39], v71, s37, v[10:11]
	v_mad_u64_u32 v[54:55], s[38:39], v74, s37, v[10:11]
	v_mad_u64_u32 v[56:57], s[38:39], v73, s37, v[10:11]
	v_mad_u64_u32 v[58:59], s[38:39], v76, s37, v[10:11]
	v_mad_u64_u32 v[60:61], s[38:39], v75, s37, v[10:11]
	v_mad_u64_u32 v[62:63], s[38:39], v78, s37, v[10:11]
	v_mad_u64_u32 v[64:65], s[38:39], v77, s37, v[10:11]
	s_lshl_b32 s38, s21, 1
	s_lshl_b32 s39, s25, 1
	v_or_b32_e32 v112, s38, v1
	v_or_b32_e32 v113, s39, v6
	s_add_i32 s40, s38, 4
	s_add_i32 s41, s39, 4
	s_add_i32 s42, s38, 8
	s_add_i32 s43, s39, 8
	s_add_i32 s44, s38, 12
	s_add_i32 s45, s39, 12
	s_add_i32 s46, s38, 16
	s_add_i32 s47, s39, 16
	s_add_i32 s48, s38, 20
	s_add_i32 s49, s39, 20
	s_add_i32 s50, s38, 24
	s_add_i32 s51, s39, 24
	s_add_i32 s38, s38, 28
	s_add_i32 s39, s39, 28
	v_add_u32_e32 v116, s24, v113
	v_or_b32_e32 v114, s40, v1
	v_or_b32_e32 v146, s41, v6
	v_or_b32_e32 v147, s42, v1
	v_or_b32_e32 v148, s43, v6
	v_or_b32_e32 v149, s44, v1
	v_or_b32_e32 v150, s45, v6
	v_or_b32_e32 v151, s46, v1
	v_or_b32_e32 v152, s47, v6
	v_or_b32_e32 v153, s48, v1
	v_or_b32_e32 v154, s49, v6
	v_or_b32_e32 v155, s50, v1
	v_or_b32_e32 v156, s51, v6
	v_or_b32_e32 v157, s38, v1
	v_or_b32_e32 v158, s39, v6
	v_add_u32_e32 v110, s20, v112
	v_ashrrev_i32_e32 v117, 31, v116
	v_add_u32_e32 v118, s20, v114
	v_add_u32_e32 v120, s24, v146
	v_add_u32_e32 v122, s20, v147
	v_add_u32_e32 v124, s24, v148
	v_add_u32_e32 v126, s20, v149
	v_add_u32_e32 v128, s24, v150
	v_add_u32_e32 v130, s20, v151
	v_add_u32_e32 v132, s24, v152
	v_add_u32_e32 v134, s20, v153
	v_add_u32_e32 v136, s24, v154
	v_add_u32_e32 v138, s20, v155
	v_add_u32_e32 v140, s24, v156
	v_add_u32_e32 v142, s20, v157
	v_add_u32_e32 v144, s24, v158
	v_ashrrev_i32_e32 v111, 31, v110
	v_lshlrev_b64 v[116:117], 12, v[116:117]
	v_ashrrev_i32_e32 v121, 31, v120
	v_ashrrev_i32_e32 v119, 31, v118
	v_ashrrev_i32_e32 v125, 31, v124
	v_ashrrev_i32_e32 v123, 31, v122
	v_ashrrev_i32_e32 v129, 31, v128
	v_ashrrev_i32_e32 v127, 31, v126
	v_ashrrev_i32_e32 v133, 31, v132
	v_ashrrev_i32_e32 v131, 31, v130
	v_ashrrev_i32_e32 v137, 31, v136
	v_ashrrev_i32_e32 v135, 31, v134
	v_ashrrev_i32_e32 v141, 31, v140
	v_ashrrev_i32_e32 v139, 31, v138
	v_ashrrev_i32_e32 v145, 31, v144
	v_ashrrev_i32_e32 v143, 31, v142
	v_lshlrev_b64 v[110:111], 12, v[110:111]
	v_lshl_add_u64 v[116:117], v[2:3], 0, v[116:117]
	v_lshlrev_b64 v[118:119], 12, v[118:119]
	v_lshlrev_b64 v[120:121], 12, v[120:121]
	v_lshlrev_b64 v[122:123], 12, v[122:123]
	v_lshlrev_b64 v[124:125], 12, v[124:125]
	v_lshlrev_b64 v[126:127], 12, v[126:127]
	v_lshlrev_b64 v[128:129], 12, v[128:129]
	v_lshlrev_b64 v[130:131], 12, v[130:131]
	v_lshlrev_b64 v[132:133], 12, v[132:133]
	v_lshlrev_b64 v[134:135], 12, v[134:135]
	v_lshlrev_b64 v[136:137], 12, v[136:137]
	v_lshlrev_b64 v[138:139], 12, v[138:139]
	v_lshlrev_b64 v[140:141], 12, v[140:141]
	v_lshlrev_b64 v[142:143], 12, v[142:143]
	v_lshlrev_b64 v[144:145], 12, v[144:145]
	v_lshl_add_u64 v[110:111], v[2:3], 0, v[110:111]
	v_lshl_add_u64 v[120:121], v[2:3], 0, v[120:121]
	v_lshl_add_u64 v[118:119], v[2:3], 0, v[118:119]
	v_lshl_add_u64 v[124:125], v[2:3], 0, v[124:125]
	v_lshl_add_u64 v[122:123], v[2:3], 0, v[122:123]
	v_lshl_add_u64 v[128:129], v[2:3], 0, v[128:129]
	v_lshl_add_u64 v[126:127], v[2:3], 0, v[126:127]
	v_lshl_add_u64 v[132:133], v[2:3], 0, v[132:133]
	v_lshl_add_u64 v[130:131], v[2:3], 0, v[130:131]
	v_lshl_add_u64 v[136:137], v[2:3], 0, v[136:137]
	v_lshl_add_u64 v[134:135], v[2:3], 0, v[134:135]
	v_lshl_add_u64 v[140:141], v[2:3], 0, v[140:141]
	v_lshl_add_u64 v[138:139], v[2:3], 0, v[138:139]
	v_lshl_add_u64 v[144:145], v[2:3], 0, v[144:145]
	v_lshl_add_u64 v[142:143], v[2:3], 0, v[142:143]
	global_load_dword v159, v[116:117], off
	global_load_dword v160, v[110:111], off
	global_load_dword v161, v[120:121], off
	global_load_dword v162, v[118:119], off
	global_load_dword v163, v[124:125], off
	global_load_dword v164, v[122:123], off
	global_load_dword v165, v[128:129], off
	global_load_dword v166, v[126:127], off
	global_load_dword v167, v[132:133], off
	global_load_dword v168, v[130:131], off
	global_load_dword v169, v[136:137], off
	global_load_dword v170, v[134:135], off
	global_load_dword v171, v[140:141], off
	global_load_dword v172, v[138:139], off
	global_load_dword v173, v[144:145], off
	global_load_dword v174, v[142:143], off
	s_add_i32 s25, s25, 16
	s_add_i32 s21, s21, 16
	s_add_i32 s31, s31, -16
	v_mad_u64_u32 v[110:111], s[38:39], v113, s37, v[10:11]
	s_cmp_lg_u32 s31, 0
	v_mad_u64_u32 v[116:117], s[38:39], v112, s37, v[10:11]
	v_mad_u64_u32 v[118:119], s[38:39], v146, s37, v[10:11]
	v_mad_u64_u32 v[120:121], s[38:39], v114, s37, v[10:11]
	v_mad_u64_u32 v[122:123], s[38:39], v148, s37, v[10:11]
	v_mad_u64_u32 v[124:125], s[38:39], v147, s37, v[10:11]
	v_mad_u64_u32 v[126:127], s[38:39], v150, s37, v[10:11]
	v_mad_u64_u32 v[128:129], s[38:39], v149, s37, v[10:11]
	v_mad_u64_u32 v[130:131], s[38:39], v152, s37, v[10:11]
	v_mad_u64_u32 v[132:133], s[38:39], v151, s37, v[10:11]
	v_mad_u64_u32 v[134:135], s[38:39], v154, s37, v[10:11]
	v_mad_u64_u32 v[136:137], s[38:39], v153, s37, v[10:11]
	v_mad_u64_u32 v[138:139], s[38:39], v156, s37, v[10:11]
	v_mad_u64_u32 v[140:141], s[38:39], v155, s37, v[10:11]
	v_mad_u64_u32 v[142:143], s[38:39], v158, s37, v[10:11]
	v_mad_u64_u32 v[144:145], s[38:39], v157, s37, v[10:11]
	s_waitcnt vmcnt(31)
	ds_write_b32 v4, v79
	s_waitcnt vmcnt(30)
	ds_write_b32 v32, v80
	s_waitcnt vmcnt(29)
	ds_write_b32 v34, v81
	s_waitcnt vmcnt(28)
	ds_write_b32 v40, v82
	s_waitcnt vmcnt(27)
	ds_write_b32 v42, v83
	s_waitcnt vmcnt(26)
	ds_write_b32 v44, v84
	s_waitcnt vmcnt(25)
	ds_write_b32 v46, v85
	s_waitcnt vmcnt(24)
	ds_write_b32 v48, v86
	s_waitcnt vmcnt(23)
	ds_write_b32 v50, v87
	s_waitcnt vmcnt(22)
	ds_write_b32 v52, v88
	s_waitcnt vmcnt(21)
	ds_write_b32 v54, v89
	s_waitcnt vmcnt(20)
	ds_write_b32 v56, v90
	s_waitcnt vmcnt(19)
	ds_write_b32 v58, v91
	s_waitcnt vmcnt(18)
	ds_write_b32 v60, v92
	s_waitcnt vmcnt(17)
	ds_write_b32 v62, v93
	s_waitcnt vmcnt(16)
	ds_write_b32 v64, v94
	s_waitcnt vmcnt(15)
	ds_write_b32 v110, v159
	s_waitcnt vmcnt(14)
	ds_write_b32 v116, v160
	s_waitcnt vmcnt(13)
	ds_write_b32 v118, v161
	s_waitcnt vmcnt(12)
	ds_write_b32 v120, v162
	s_waitcnt vmcnt(11)
	ds_write_b32 v122, v163
	s_waitcnt vmcnt(10)
	ds_write_b32 v124, v164
	s_waitcnt vmcnt(9)
	ds_write_b32 v126, v165
	s_waitcnt vmcnt(8)
	ds_write_b32 v128, v166
	s_waitcnt vmcnt(7)
	ds_write_b32 v130, v167
	s_waitcnt vmcnt(6)
	ds_write_b32 v132, v168
	s_waitcnt vmcnt(5)
	ds_write_b32 v134, v169
	s_waitcnt vmcnt(4)
	ds_write_b32 v136, v170
	s_waitcnt vmcnt(3)
	ds_write_b32 v138, v171
	s_waitcnt vmcnt(2)
	ds_write_b32 v140, v172
	s_waitcnt vmcnt(1)
	ds_write_b32 v142, v173
	s_waitcnt vmcnt(0)
	ds_write_b32 v144, v174

.LBB0_215:
	s_lshl_b32 s40, s38, 1
	s_lshl_b32 s41, s19, 1
	v_or_b32_e32 v11, s40, v1
	v_or_b32_e32 v64, s41, v6
	s_add_i32 s42, s40, 4
	s_add_i32 s43, s41, 4
	s_add_i32 s44, s40, 8
	s_add_i32 s45, s41, 8
	s_add_i32 s46, s40, 12
	s_add_i32 s47, s41, 12
	s_add_i32 s48, s40, 16
	s_add_i32 s49, s41, 16
	s_add_i32 s50, s40, 20
	s_add_i32 s51, s41, 20
	s_add_i32 s52, s40, 24
	s_add_i32 s53, s41, 24
	s_add_i32 s40, s40, 28
	s_add_i32 s41, s41, 28
	v_add_u32_e32 v4, s18, v64
	v_or_b32_e32 v65, s42, v1
	v_or_b32_e32 v66, s43, v6
	v_or_b32_e32 v67, s44, v1
	v_or_b32_e32 v68, s45, v6
	v_or_b32_e32 v69, s46, v1
	v_or_b32_e32 v70, s47, v6
	v_or_b32_e32 v71, s48, v1
	v_or_b32_e32 v72, s49, v6
	v_or_b32_e32 v73, s50, v1
	v_or_b32_e32 v74, s51, v6
	v_or_b32_e32 v75, s52, v1
	v_or_b32_e32 v76, s53, v6
	v_or_b32_e32 v77, s40, v1
	v_or_b32_e32 v78, s41, v6
	v_add_u32_e32 v30, s23, v11
	v_mad_i64_i32 v[4:5], s[40:41], v4, s30, v[2:3]
	v_add_u32_e32 v34, s23, v65
	v_add_u32_e32 v32, s18, v66
	v_add_u32_e32 v42, s23, v67
	v_add_u32_e32 v40, s18, v68
	v_add_u32_e32 v46, s23, v69
	v_add_u32_e32 v44, s18, v70
	v_add_u32_e32 v50, s23, v71
	v_add_u32_e32 v48, s18, v72
	v_add_u32_e32 v54, s23, v73
	v_add_u32_e32 v52, s18, v74
	v_add_u32_e32 v58, s23, v75
	v_add_u32_e32 v56, s18, v76
	v_add_u32_e32 v62, s23, v77
	v_add_u32_e32 v60, s18, v78
	v_mad_i64_i32 v[30:31], s[40:41], v30, s30, v[2:3]
	v_mad_i64_i32 v[32:33], s[40:41], v32, s30, v[2:3]
	v_mad_i64_i32 v[34:35], s[40:41], v34, s30, v[2:3]
	v_mad_i64_i32 v[40:41], s[40:41], v40, s30, v[2:3]
	v_mad_i64_i32 v[42:43], s[40:41], v42, s30, v[2:3]
	v_mad_i64_i32 v[44:45], s[40:41], v44, s30, v[2:3]
	v_mad_i64_i32 v[46:47], s[40:41], v46, s30, v[2:3]
	v_mad_i64_i32 v[48:49], s[40:41], v48, s30, v[2:3]
	v_mad_i64_i32 v[50:51], s[40:41], v50, s30, v[2:3]
	v_mad_i64_i32 v[52:53], s[40:41], v52, s30, v[2:3]
	v_mad_i64_i32 v[54:55], s[40:41], v54, s30, v[2:3]
	v_mad_i64_i32 v[56:57], s[40:41], v56, s30, v[2:3]
	v_mad_i64_i32 v[58:59], s[40:41], v58, s30, v[2:3]
	v_mad_i64_i32 v[60:61], s[40:41], v60, s30, v[2:3]
	v_mad_i64_i32 v[62:63], s[40:41], v62, s30, v[2:3]
	global_load_dword v79, v[4:5], off
	global_load_dword v80, v[30:31], off
	global_load_dword v81, v[32:33], off
	global_load_dword v82, v[34:35], off
	global_load_dword v83, v[40:41], off
	global_load_dword v84, v[42:43], off
	global_load_dword v85, v[44:45], off
	global_load_dword v86, v[46:47], off
	global_load_dword v87, v[48:49], off
	global_load_dword v88, v[50:51], off
	global_load_dword v89, v[52:53], off
	global_load_dword v90, v[54:55], off
	global_load_dword v91, v[56:57], off
	global_load_dword v92, v[58:59], off
	global_load_dword v93, v[60:61], off
	global_load_dword v94, v[62:63], off
	s_add_i32 s19, s19, 16
	s_add_i32 s38, s38, 16
	s_add_i32 s39, s39, -16
	v_mad_u64_u32 v[4:5], s[40:41], v64, s31, v[10:11]
	s_cmp_lg_u32 s39, 0
	v_mad_u64_u32 v[30:31], s[40:41], v11, s31, v[10:11]
	v_mad_u64_u32 v[32:33], s[40:41], v66, s31, v[10:11]
	v_mad_u64_u32 v[34:35], s[40:41], v65, s31, v[10:11]
	v_mad_u64_u32 v[40:41], s[40:41], v68, s31, v[10:11]
	v_mad_u64_u32 v[42:43], s[40:41], v67, s31, v[10:11]
	v_mad_u64_u32 v[44:45], s[40:41], v70, s31, v[10:11]
	v_mad_u64_u32 v[46:47], s[40:41], v69, s31, v[10:11]
	v_mad_u64_u32 v[48:49], s[40:41], v72, s31, v[10:11]
	v_mad_u64_u32 v[50:51], s[40:41], v71, s31, v[10:11]
	v_mad_u64_u32 v[52:53], s[40:41], v74, s31, v[10:11]
	v_mad_u64_u32 v[54:55], s[40:41], v73, s31, v[10:11]
	v_mad_u64_u32 v[56:57], s[40:41], v76, s31, v[10:11]
	v_mad_u64_u32 v[58:59], s[40:41], v75, s31, v[10:11]
	v_mad_u64_u32 v[60:61], s[40:41], v78, s31, v[10:11]
	v_mad_u64_u32 v[62:63], s[40:41], v77, s31, v[10:11]
	s_lshl_b32 s40, s38, 1
	s_lshl_b32 s41, s19, 1
	v_or_b32_e32 v112, s40, v1
	v_or_b32_e32 v144, s41, v6
	s_add_i32 s42, s40, 4
	s_add_i32 s43, s41, 4
	s_add_i32 s44, s40, 8
	s_add_i32 s45, s41, 8
	s_add_i32 s46, s40, 12
	s_add_i32 s47, s41, 12
	s_add_i32 s48, s40, 16
	s_add_i32 s49, s41, 16
	s_add_i32 s50, s40, 20
	s_add_i32 s51, s41, 20
	s_add_i32 s52, s40, 24
	s_add_i32 s53, s41, 24
	s_add_i32 s40, s40, 28
	s_add_i32 s41, s41, 28
	v_add_u32_e32 v110, s18, v144
	v_or_b32_e32 v145, s42, v1
	v_or_b32_e32 v146, s43, v6
	v_or_b32_e32 v147, s44, v1
	v_or_b32_e32 v148, s45, v6
	v_or_b32_e32 v149, s46, v1
	v_or_b32_e32 v150, s47, v6
	v_or_b32_e32 v151, s48, v1
	v_or_b32_e32 v152, s49, v6
	v_or_b32_e32 v153, s50, v1
	v_or_b32_e32 v154, s51, v6
	v_or_b32_e32 v155, s52, v1
	v_or_b32_e32 v156, s53, v6
	v_or_b32_e32 v157, s40, v1
	v_or_b32_e32 v158, s41, v6
	v_add_u32_e32 v114, s23, v112
	v_mad_i64_i32 v[110:111], s[40:41], v110, s30, v[2:3]
	v_add_u32_e32 v118, s23, v145
	v_add_u32_e32 v116, s18, v146
	v_add_u32_e32 v122, s23, v147
	v_add_u32_e32 v120, s18, v148
	v_add_u32_e32 v126, s23, v149
	v_add_u32_e32 v124, s18, v150
	v_add_u32_e32 v130, s23, v151
	v_add_u32_e32 v128, s18, v152
	v_add_u32_e32 v134, s23, v153
	v_add_u32_e32 v132, s18, v154
	v_add_u32_e32 v138, s23, v155
	v_add_u32_e32 v136, s18, v156
	v_add_u32_e32 v142, s23, v157
	v_add_u32_e32 v140, s18, v158
	v_mad_i64_i32 v[114:115], s[40:41], v114, s30, v[2:3]
	v_mad_i64_i32 v[116:117], s[40:41], v116, s30, v[2:3]
	v_mad_i64_i32 v[118:119], s[40:41], v118, s30, v[2:3]
	v_mad_i64_i32 v[120:121], s[40:41], v120, s30, v[2:3]
	v_mad_i64_i32 v[122:123], s[40:41], v122, s30, v[2:3]
	v_mad_i64_i32 v[124:125], s[40:41], v124, s30, v[2:3]
	v_mad_i64_i32 v[126:127], s[40:41], v126, s30, v[2:3]
	v_mad_i64_i32 v[128:129], s[40:41], v128, s30, v[2:3]
	v_mad_i64_i32 v[130:131], s[40:41], v130, s30, v[2:3]
	v_mad_i64_i32 v[132:133], s[40:41], v132, s30, v[2:3]
	v_mad_i64_i32 v[134:135], s[40:41], v134, s30, v[2:3]
	v_mad_i64_i32 v[136:137], s[40:41], v136, s30, v[2:3]
	v_mad_i64_i32 v[138:139], s[40:41], v138, s30, v[2:3]
	v_mad_i64_i32 v[140:141], s[40:41], v140, s30, v[2:3]
	v_mad_i64_i32 v[142:143], s[40:41], v142, s30, v[2:3]
	global_load_dword v159, v[110:111], off
	global_load_dword v160, v[114:115], off
	global_load_dword v161, v[116:117], off
	global_load_dword v162, v[118:119], off
	global_load_dword v163, v[120:121], off
	global_load_dword v164, v[122:123], off
	global_load_dword v165, v[124:125], off
	global_load_dword v166, v[126:127], off
	global_load_dword v167, v[128:129], off
	global_load_dword v168, v[130:131], off
	global_load_dword v169, v[132:133], off
	global_load_dword v170, v[134:135], off
	global_load_dword v171, v[136:137], off
	global_load_dword v172, v[138:139], off
	global_load_dword v173, v[140:141], off
	global_load_dword v174, v[142:143], off
	s_add_i32 s19, s19, 16
	s_add_i32 s38, s38, 16
	s_add_i32 s39, s39, -16
	v_mad_u64_u32 v[110:111], s[40:41], v144, s31, v[10:11]
	s_cmp_lg_u32 s39, 0
	v_mad_u64_u32 v[114:115], s[40:41], v112, s31, v[10:11]
	v_mad_u64_u32 v[116:117], s[40:41], v146, s31, v[10:11]
	v_mad_u64_u32 v[118:119], s[40:41], v145, s31, v[10:11]
	v_mad_u64_u32 v[120:121], s[40:41], v148, s31, v[10:11]
	v_mad_u64_u32 v[122:123], s[40:41], v147, s31, v[10:11]
	v_mad_u64_u32 v[124:125], s[40:41], v150, s31, v[10:11]
	v_mad_u64_u32 v[126:127], s[40:41], v149, s31, v[10:11]
	v_mad_u64_u32 v[128:129], s[40:41], v152, s31, v[10:11]
	v_mad_u64_u32 v[130:131], s[40:41], v151, s31, v[10:11]
	v_mad_u64_u32 v[132:133], s[40:41], v154, s31, v[10:11]
	v_mad_u64_u32 v[134:135], s[40:41], v153, s31, v[10:11]
	v_mad_u64_u32 v[136:137], s[40:41], v156, s31, v[10:11]
	v_mad_u64_u32 v[138:139], s[40:41], v155, s31, v[10:11]
	v_mad_u64_u32 v[140:141], s[40:41], v158, s31, v[10:11]
	v_mad_u64_u32 v[142:143], s[40:41], v157, s31, v[10:11]
	s_waitcnt vmcnt(31)
	ds_write_b32 v4, v79
	s_waitcnt vmcnt(30)
	ds_write_b32 v30, v80
	s_waitcnt vmcnt(29)
	ds_write_b32 v32, v81
	s_waitcnt vmcnt(28)
	ds_write_b32 v34, v82
	s_waitcnt vmcnt(27)
	ds_write_b32 v40, v83
	s_waitcnt vmcnt(26)
	ds_write_b32 v42, v84
	s_waitcnt vmcnt(25)
	ds_write_b32 v44, v85
	s_waitcnt vmcnt(24)
	ds_write_b32 v46, v86
	s_waitcnt vmcnt(23)
	ds_write_b32 v48, v87
	s_waitcnt vmcnt(22)
	ds_write_b32 v50, v88
	s_waitcnt vmcnt(21)
	ds_write_b32 v52, v89
	s_waitcnt vmcnt(20)
	ds_write_b32 v54, v90
	s_waitcnt vmcnt(19)
	ds_write_b32 v56, v91
	s_waitcnt vmcnt(18)
	ds_write_b32 v58, v92
	s_waitcnt vmcnt(17)
	ds_write_b32 v60, v93
	s_waitcnt vmcnt(16)
	ds_write_b32 v62, v94
	s_waitcnt vmcnt(15)
	ds_write_b32 v110, v159
	s_waitcnt vmcnt(14)
	ds_write_b32 v114, v160
	s_waitcnt vmcnt(13)
	ds_write_b32 v116, v161
	s_waitcnt vmcnt(12)
	ds_write_b32 v118, v162
	s_waitcnt vmcnt(11)
	ds_write_b32 v120, v163
	s_waitcnt vmcnt(10)
	ds_write_b32 v122, v164
	s_waitcnt vmcnt(9)
	ds_write_b32 v124, v165
	s_waitcnt vmcnt(8)
	ds_write_b32 v126, v166
	s_waitcnt vmcnt(7)
	ds_write_b32 v128, v167
	s_waitcnt vmcnt(6)
	ds_write_b32 v130, v168
	s_waitcnt vmcnt(5)
	ds_write_b32 v132, v169
	s_waitcnt vmcnt(4)
	ds_write_b32 v134, v170
	s_waitcnt vmcnt(3)
	ds_write_b32 v136, v171
	s_waitcnt vmcnt(2)
	ds_write_b32 v138, v172
	s_waitcnt vmcnt(1)
	ds_write_b32 v140, v173
	s_waitcnt vmcnt(0)
	ds_write_b32 v142, v174

.LBB0_229:
	s_lshl_b32 s36, s33, 1
	s_lshl_b32 s37, s34, 1
	v_or_b32_e32 v11, s36, v1
	v_or_b32_e32 v66, s37, v6
	s_add_i32 s38, s36, 4
	s_add_i32 s39, s37, 4
	s_add_i32 s40, s36, 8
	s_add_i32 s41, s37, 8
	s_add_i32 s42, s36, 12
	s_add_i32 s43, s37, 12
	s_add_i32 s44, s36, 16
	s_add_i32 s45, s37, 16
	s_add_i32 s46, s36, 20
	s_add_i32 s47, s37, 20
	s_add_i32 s48, s36, 24
	s_add_i32 s49, s37, 24
	s_add_i32 s36, s36, 28
	s_add_i32 s37, s37, 28
	v_add_u32_e32 v32, s16, v66
	v_or_b32_e32 v67, s38, v1
	v_or_b32_e32 v68, s39, v6
	v_or_b32_e32 v69, s40, v1
	v_or_b32_e32 v70, s41, v6
	v_or_b32_e32 v71, s42, v1
	v_or_b32_e32 v72, s43, v6
	v_or_b32_e32 v73, s44, v1
	v_or_b32_e32 v74, s45, v6
	v_or_b32_e32 v75, s46, v1
	v_or_b32_e32 v76, s47, v6
	v_or_b32_e32 v77, s48, v1
	v_or_b32_e32 v78, s49, v6
	v_or_b32_e32 v79, s36, v1
	v_or_b32_e32 v80, s37, v6
	v_add_u32_e32 v4, s23, v11
	v_ashrrev_i32_e32 v33, 31, v32
	v_add_u32_e32 v34, s23, v67
	v_add_u32_e32 v40, s16, v68
	v_add_u32_e32 v42, s23, v69
	v_add_u32_e32 v44, s16, v70
	v_add_u32_e32 v46, s23, v71
	v_add_u32_e32 v48, s16, v72
	v_add_u32_e32 v50, s23, v73
	v_add_u32_e32 v52, s16, v74
	v_add_u32_e32 v54, s23, v75
	v_add_u32_e32 v56, s16, v76
	v_add_u32_e32 v58, s23, v77
	v_add_u32_e32 v60, s16, v78
	v_add_u32_e32 v62, s23, v79
	v_add_u32_e32 v64, s16, v80
	v_ashrrev_i32_e32 v5, 31, v4
	v_lshlrev_b64 v[32:33], 12, v[32:33]
	v_ashrrev_i32_e32 v41, 31, v40
	v_ashrrev_i32_e32 v35, 31, v34
	v_ashrrev_i32_e32 v45, 31, v44
	v_ashrrev_i32_e32 v43, 31, v42
	v_ashrrev_i32_e32 v49, 31, v48
	v_ashrrev_i32_e32 v47, 31, v46
	v_ashrrev_i32_e32 v53, 31, v52
	v_ashrrev_i32_e32 v51, 31, v50
	v_ashrrev_i32_e32 v57, 31, v56
	v_ashrrev_i32_e32 v55, 31, v54
	v_ashrrev_i32_e32 v61, 31, v60
	v_ashrrev_i32_e32 v59, 31, v58
	v_ashrrev_i32_e32 v65, 31, v64
	v_ashrrev_i32_e32 v63, 31, v62
	v_lshlrev_b64 v[4:5], 12, v[4:5]
	v_lshl_add_u64 v[32:33], v[2:3], 0, v[32:33]
	v_lshlrev_b64 v[34:35], 12, v[34:35]
	v_lshlrev_b64 v[40:41], 12, v[40:41]
	v_lshlrev_b64 v[42:43], 12, v[42:43]
	v_lshlrev_b64 v[44:45], 12, v[44:45]
	v_lshlrev_b64 v[46:47], 12, v[46:47]
	v_lshlrev_b64 v[48:49], 12, v[48:49]
	v_lshlrev_b64 v[50:51], 12, v[50:51]
	v_lshlrev_b64 v[52:53], 12, v[52:53]
	v_lshlrev_b64 v[54:55], 12, v[54:55]
	v_lshlrev_b64 v[56:57], 12, v[56:57]
	v_lshlrev_b64 v[58:59], 12, v[58:59]
	v_lshlrev_b64 v[60:61], 12, v[60:61]
	v_lshlrev_b64 v[62:63], 12, v[62:63]
	v_lshlrev_b64 v[64:65], 12, v[64:65]
	v_lshl_add_u64 v[4:5], v[2:3], 0, v[4:5]
	v_lshl_add_u64 v[40:41], v[2:3], 0, v[40:41]
	v_lshl_add_u64 v[34:35], v[2:3], 0, v[34:35]
	v_lshl_add_u64 v[44:45], v[2:3], 0, v[44:45]
	v_lshl_add_u64 v[42:43], v[2:3], 0, v[42:43]
	v_lshl_add_u64 v[48:49], v[2:3], 0, v[48:49]
	v_lshl_add_u64 v[46:47], v[2:3], 0, v[46:47]
	v_lshl_add_u64 v[52:53], v[2:3], 0, v[52:53]
	v_lshl_add_u64 v[50:51], v[2:3], 0, v[50:51]
	v_lshl_add_u64 v[56:57], v[2:3], 0, v[56:57]
	v_lshl_add_u64 v[54:55], v[2:3], 0, v[54:55]
	v_lshl_add_u64 v[60:61], v[2:3], 0, v[60:61]
	v_lshl_add_u64 v[58:59], v[2:3], 0, v[58:59]
	v_lshl_add_u64 v[64:65], v[2:3], 0, v[64:65]
	v_lshl_add_u64 v[62:63], v[2:3], 0, v[62:63]
	global_load_dword v81, v[32:33], off
	global_load_dword v82, v[4:5], off
	global_load_dword v83, v[40:41], off
	global_load_dword v84, v[34:35], off
	global_load_dword v85, v[44:45], off
	global_load_dword v86, v[42:43], off
	global_load_dword v87, v[48:49], off
	global_load_dword v88, v[46:47], off
	global_load_dword v89, v[52:53], off
	global_load_dword v90, v[50:51], off
	global_load_dword v91, v[56:57], off
	global_load_dword v92, v[54:55], off
	global_load_dword v93, v[60:61], off
	global_load_dword v94, v[58:59], off
	global_load_dword v95, v[64:65], off
	global_load_dword v96, v[62:63], off
	s_add_i32 s34, s34, 16
	s_add_i32 s33, s33, 16
	s_add_i32 s35, s35, -16
	v_mad_u64_u32 v[4:5], s[36:37], v66, s31, v[10:11]
	s_cmp_lg_u32 s35, 0
	v_mad_u64_u32 v[32:33], s[36:37], v11, s31, v[10:11]
	v_mad_u64_u32 v[34:35], s[36:37], v68, s31, v[10:11]
	v_mad_u64_u32 v[40:41], s[36:37], v67, s31, v[10:11]
	v_mad_u64_u32 v[42:43], s[36:37], v70, s31, v[10:11]
	v_mad_u64_u32 v[44:45], s[36:37], v69, s31, v[10:11]
	v_mad_u64_u32 v[46:47], s[36:37], v72, s31, v[10:11]
	v_mad_u64_u32 v[48:49], s[36:37], v71, s31, v[10:11]
	v_mad_u64_u32 v[50:51], s[36:37], v74, s31, v[10:11]
	v_mad_u64_u32 v[52:53], s[36:37], v73, s31, v[10:11]
	v_mad_u64_u32 v[54:55], s[36:37], v76, s31, v[10:11]
	v_mad_u64_u32 v[56:57], s[36:37], v75, s31, v[10:11]
	v_mad_u64_u32 v[58:59], s[36:37], v78, s31, v[10:11]
	v_mad_u64_u32 v[60:61], s[36:37], v77, s31, v[10:11]
	v_mad_u64_u32 v[62:63], s[36:37], v80, s31, v[10:11]
	v_mad_u64_u32 v[64:65], s[36:37], v79, s31, v[10:11]
	s_lshl_b32 s36, s33, 1
	s_lshl_b32 s37, s34, 1
	v_or_b32_e32 v112, s36, v1
	v_or_b32_e32 v144, s37, v6
	s_add_i32 s38, s36, 4
	s_add_i32 s39, s37, 4
	s_add_i32 s40, s36, 8
	s_add_i32 s41, s37, 8
	s_add_i32 s42, s36, 12
	s_add_i32 s43, s37, 12
	s_add_i32 s44, s36, 16
	s_add_i32 s45, s37, 16
	s_add_i32 s46, s36, 20
	s_add_i32 s47, s37, 20
	s_add_i32 s48, s36, 24
	s_add_i32 s49, s37, 24
	s_add_i32 s36, s36, 28
	s_add_i32 s37, s37, 28
	v_add_u32_e32 v114, s16, v144
	v_or_b32_e32 v145, s38, v1
	v_or_b32_e32 v146, s39, v6
	v_or_b32_e32 v147, s40, v1
	v_or_b32_e32 v148, s41, v6
	v_or_b32_e32 v149, s42, v1
	v_or_b32_e32 v150, s43, v6
	v_or_b32_e32 v151, s44, v1
	v_or_b32_e32 v152, s45, v6
	v_or_b32_e32 v153, s46, v1
	v_or_b32_e32 v154, s47, v6
	v_or_b32_e32 v155, s48, v1
	v_or_b32_e32 v156, s49, v6
	v_or_b32_e32 v157, s36, v1
	v_or_b32_e32 v158, s37, v6
	v_add_u32_e32 v110, s23, v112
	v_ashrrev_i32_e32 v115, 31, v114
	v_add_u32_e32 v116, s23, v145
	v_add_u32_e32 v118, s16, v146
	v_add_u32_e32 v120, s23, v147
	v_add_u32_e32 v122, s16, v148
	v_add_u32_e32 v124, s23, v149
	v_add_u32_e32 v126, s16, v150
	v_add_u32_e32 v128, s23, v151
	v_add_u32_e32 v130, s16, v152
	v_add_u32_e32 v132, s23, v153
	v_add_u32_e32 v134, s16, v154
	v_add_u32_e32 v136, s23, v155
	v_add_u32_e32 v138, s16, v156
	v_add_u32_e32 v140, s23, v157
	v_add_u32_e32 v142, s16, v158
	v_ashrrev_i32_e32 v111, 31, v110
	v_lshlrev_b64 v[114:115], 12, v[114:115]
	v_ashrrev_i32_e32 v119, 31, v118
	v_ashrrev_i32_e32 v117, 31, v116
	v_ashrrev_i32_e32 v123, 31, v122
	v_ashrrev_i32_e32 v121, 31, v120
	v_ashrrev_i32_e32 v127, 31, v126
	v_ashrrev_i32_e32 v125, 31, v124
	v_ashrrev_i32_e32 v131, 31, v130
	v_ashrrev_i32_e32 v129, 31, v128
	v_ashrrev_i32_e32 v135, 31, v134
	v_ashrrev_i32_e32 v133, 31, v132
	v_ashrrev_i32_e32 v139, 31, v138
	v_ashrrev_i32_e32 v137, 31, v136
	v_ashrrev_i32_e32 v143, 31, v142
	v_ashrrev_i32_e32 v141, 31, v140
	v_lshlrev_b64 v[110:111], 12, v[110:111]
	v_lshl_add_u64 v[114:115], v[2:3], 0, v[114:115]
	v_lshlrev_b64 v[116:117], 12, v[116:117]
	v_lshlrev_b64 v[118:119], 12, v[118:119]
	v_lshlrev_b64 v[120:121], 12, v[120:121]
	v_lshlrev_b64 v[122:123], 12, v[122:123]
	v_lshlrev_b64 v[124:125], 12, v[124:125]
	v_lshlrev_b64 v[126:127], 12, v[126:127]
	v_lshlrev_b64 v[128:129], 12, v[128:129]
	v_lshlrev_b64 v[130:131], 12, v[130:131]
	v_lshlrev_b64 v[132:133], 12, v[132:133]
	v_lshlrev_b64 v[134:135], 12, v[134:135]
	v_lshlrev_b64 v[136:137], 12, v[136:137]
	v_lshlrev_b64 v[138:139], 12, v[138:139]
	v_lshlrev_b64 v[140:141], 12, v[140:141]
	v_lshlrev_b64 v[142:143], 12, v[142:143]
	v_lshl_add_u64 v[110:111], v[2:3], 0, v[110:111]
	v_lshl_add_u64 v[118:119], v[2:3], 0, v[118:119]
	v_lshl_add_u64 v[116:117], v[2:3], 0, v[116:117]
	v_lshl_add_u64 v[122:123], v[2:3], 0, v[122:123]
	v_lshl_add_u64 v[120:121], v[2:3], 0, v[120:121]
	v_lshl_add_u64 v[126:127], v[2:3], 0, v[126:127]
	v_lshl_add_u64 v[124:125], v[2:3], 0, v[124:125]
	v_lshl_add_u64 v[130:131], v[2:3], 0, v[130:131]
	v_lshl_add_u64 v[128:129], v[2:3], 0, v[128:129]
	v_lshl_add_u64 v[134:135], v[2:3], 0, v[134:135]
	v_lshl_add_u64 v[132:133], v[2:3], 0, v[132:133]
	v_lshl_add_u64 v[138:139], v[2:3], 0, v[138:139]
	v_lshl_add_u64 v[136:137], v[2:3], 0, v[136:137]
	v_lshl_add_u64 v[142:143], v[2:3], 0, v[142:143]
	v_lshl_add_u64 v[140:141], v[2:3], 0, v[140:141]
	global_load_dword v159, v[114:115], off
	global_load_dword v160, v[110:111], off
	global_load_dword v161, v[118:119], off
	global_load_dword v162, v[116:117], off
	global_load_dword v163, v[122:123], off
	global_load_dword v164, v[120:121], off
	global_load_dword v165, v[126:127], off
	global_load_dword v166, v[124:125], off
	global_load_dword v167, v[130:131], off
	global_load_dword v168, v[128:129], off
	global_load_dword v169, v[134:135], off
	global_load_dword v170, v[132:133], off
	global_load_dword v171, v[138:139], off
	global_load_dword v172, v[136:137], off
	global_load_dword v173, v[142:143], off
	global_load_dword v174, v[140:141], off
	s_add_i32 s34, s34, 16
	s_add_i32 s33, s33, 16
	s_add_i32 s35, s35, -16
	v_mad_u64_u32 v[110:111], s[36:37], v144, s31, v[10:11]
	s_cmp_lg_u32 s35, 0
	v_mad_u64_u32 v[114:115], s[36:37], v112, s31, v[10:11]
	v_mad_u64_u32 v[116:117], s[36:37], v146, s31, v[10:11]
	v_mad_u64_u32 v[118:119], s[36:37], v145, s31, v[10:11]
	v_mad_u64_u32 v[120:121], s[36:37], v148, s31, v[10:11]
	v_mad_u64_u32 v[122:123], s[36:37], v147, s31, v[10:11]
	v_mad_u64_u32 v[124:125], s[36:37], v150, s31, v[10:11]
	v_mad_u64_u32 v[126:127], s[36:37], v149, s31, v[10:11]
	v_mad_u64_u32 v[128:129], s[36:37], v152, s31, v[10:11]
	v_mad_u64_u32 v[130:131], s[36:37], v151, s31, v[10:11]
	v_mad_u64_u32 v[132:133], s[36:37], v154, s31, v[10:11]
	v_mad_u64_u32 v[134:135], s[36:37], v153, s31, v[10:11]
	v_mad_u64_u32 v[136:137], s[36:37], v156, s31, v[10:11]
	v_mad_u64_u32 v[138:139], s[36:37], v155, s31, v[10:11]
	v_mad_u64_u32 v[140:141], s[36:37], v158, s31, v[10:11]
	v_mad_u64_u32 v[142:143], s[36:37], v157, s31, v[10:11]
	s_waitcnt vmcnt(31)
	ds_write_b32 v4, v81
	s_waitcnt vmcnt(30)
	ds_write_b32 v32, v82
	s_waitcnt vmcnt(29)
	ds_write_b32 v34, v83
	s_waitcnt vmcnt(28)
	ds_write_b32 v40, v84
	s_waitcnt vmcnt(27)
	ds_write_b32 v42, v85
	s_waitcnt vmcnt(26)
	ds_write_b32 v44, v86
	s_waitcnt vmcnt(25)
	ds_write_b32 v46, v87
	s_waitcnt vmcnt(24)
	ds_write_b32 v48, v88
	s_waitcnt vmcnt(23)
	ds_write_b32 v50, v89
	s_waitcnt vmcnt(22)
	ds_write_b32 v52, v90
	s_waitcnt vmcnt(21)
	ds_write_b32 v54, v91
	s_waitcnt vmcnt(20)
	ds_write_b32 v56, v92
	s_waitcnt vmcnt(19)
	ds_write_b32 v58, v93
	s_waitcnt vmcnt(18)
	ds_write_b32 v60, v94
	s_waitcnt vmcnt(17)
	ds_write_b32 v62, v95
	s_waitcnt vmcnt(16)
	ds_write_b32 v64, v96
	s_waitcnt vmcnt(15)
	ds_write_b32 v110, v159
	s_waitcnt vmcnt(14)
	ds_write_b32 v114, v160
	s_waitcnt vmcnt(13)
	ds_write_b32 v116, v161
	s_waitcnt vmcnt(12)
	ds_write_b32 v118, v162
	s_waitcnt vmcnt(11)
	ds_write_b32 v120, v163
	s_waitcnt vmcnt(10)
	ds_write_b32 v122, v164
	s_waitcnt vmcnt(9)
	ds_write_b32 v124, v165
	s_waitcnt vmcnt(8)
	ds_write_b32 v126, v166
	s_waitcnt vmcnt(7)
	ds_write_b32 v128, v167
	s_waitcnt vmcnt(6)
	ds_write_b32 v130, v168
	s_waitcnt vmcnt(5)
	ds_write_b32 v132, v169
	s_waitcnt vmcnt(4)
	ds_write_b32 v134, v170
	s_waitcnt vmcnt(3)
	ds_write_b32 v136, v171
	s_waitcnt vmcnt(2)
	ds_write_b32 v138, v172
	s_waitcnt vmcnt(1)
	ds_write_b32 v140, v173
	s_waitcnt vmcnt(0)
	ds_write_b32 v142, v174

.LBB0_387:
	s_lshl_b32 s47, s25, 1
	s_lshl_b32 s48, s20, 1
	v_or_b32_e32 v11, s47, v1
	v_or_b32_e32 v29, s48, v8
	s_add_i32 s49, s47, 4
	s_add_i32 s50, s48, 4
	s_add_i32 s51, s47, 8
	s_add_i32 s52, s48, 8
	s_add_i32 s53, s47, 12
	s_add_i32 s54, s48, 12
	s_add_i32 s55, s47, 16
	s_add_i32 s60, s48, 16
	s_add_i32 s61, s47, 20
	s_add_i32 s62, s48, 20
	s_add_i32 s63, s47, 24
	s_add_i32 s64, s48, 24
	s_add_i32 s47, s47, 28
	s_add_i32 s48, s48, 28
	v_add_u32_e32 v6, s26, v29
	v_or_b32_e32 v60, s49, v1
	v_or_b32_e32 v61, s50, v8
	v_or_b32_e32 v62, s51, v1
	v_or_b32_e32 v63, s52, v8
	v_or_b32_e32 v64, s53, v1
	v_or_b32_e32 v65, s54, v8
	v_or_b32_e32 v66, s55, v1
	v_or_b32_e32 v67, s60, v8
	v_or_b32_e32 v68, s61, v1
	v_or_b32_e32 v69, s62, v8
	v_or_b32_e32 v70, s63, v1
	v_or_b32_e32 v71, s64, v8
	v_or_b32_e32 v72, s47, v1
	v_or_b32_e32 v73, s48, v8
	v_add_u32_e32 v30, s21, v11
	v_mad_i64_i32 v[6:7], s[48:49], v6, s31, v[4:5]
	v_add_u32_e32 v34, s21, v60
	v_add_u32_e32 v32, s26, v61
	v_add_u32_e32 v38, s21, v62
	v_add_u32_e32 v36, s26, v63
	v_add_u32_e32 v42, s21, v64
	v_add_u32_e32 v40, s26, v65
	v_add_u32_e32 v46, s21, v66
	v_add_u32_e32 v44, s26, v67
	v_add_u32_e32 v50, s21, v68
	v_add_u32_e32 v48, s26, v69
	v_add_u32_e32 v54, s21, v70
	v_add_u32_e32 v52, s26, v71
	v_add_u32_e32 v58, s21, v72
	v_add_u32_e32 v56, s26, v73
	v_mad_i64_i32 v[30:31], s[48:49], v30, s31, v[4:5]
	v_mad_i64_i32 v[32:33], s[48:49], v32, s31, v[4:5]
	v_mad_i64_i32 v[34:35], s[48:49], v34, s31, v[4:5]
	v_mad_i64_i32 v[36:37], s[48:49], v36, s31, v[4:5]
	v_mad_i64_i32 v[38:39], s[48:49], v38, s31, v[4:5]
	v_mad_i64_i32 v[40:41], s[48:49], v40, s31, v[4:5]
	v_mad_i64_i32 v[42:43], s[48:49], v42, s31, v[4:5]
	v_mad_i64_i32 v[44:45], s[48:49], v44, s31, v[4:5]
	v_mad_i64_i32 v[46:47], s[48:49], v46, s31, v[4:5]
	v_mad_i64_i32 v[48:49], s[48:49], v48, s31, v[4:5]
	v_mad_i64_i32 v[50:51], s[48:49], v50, s31, v[4:5]
	v_mad_i64_i32 v[52:53], s[48:49], v52, s31, v[4:5]
	v_mad_i64_i32 v[54:55], s[48:49], v54, s31, v[4:5]
	v_mad_i64_i32 v[56:57], s[48:49], v56, s31, v[4:5]
	v_mad_i64_i32 v[58:59], s[48:49], v58, s31, v[4:5]
	global_load_dword v74, v[6:7], off
	global_load_dword v75, v[30:31], off
	global_load_dword v76, v[32:33], off
	global_load_dword v77, v[34:35], off
	global_load_dword v78, v[36:37], off
	global_load_dword v79, v[38:39], off
	global_load_dword v80, v[40:41], off
	global_load_dword v81, v[42:43], off
	global_load_dword v82, v[44:45], off
	global_load_dword v83, v[46:47], off
	global_load_dword v84, v[48:49], off
	global_load_dword v85, v[50:51], off
	global_load_dword v86, v[52:53], off
	global_load_dword v87, v[54:55], off
	global_load_dword v88, v[56:57], off
	global_load_dword v89, v[58:59], off
	s_add_i32 s20, s20, 16
	s_add_i32 s25, s25, 16
	s_add_i32 s27, s27, -16
	v_mad_u64_u32 v[6:7], s[48:49], v29, s33, v[10:11]
	s_cmp_lg_u32 s27, 0
	v_mad_u64_u32 v[30:31], s[48:49], v11, s33, v[10:11]
	v_mad_u64_u32 v[32:33], s[48:49], v61, s33, v[10:11]
	v_mad_u64_u32 v[34:35], s[48:49], v60, s33, v[10:11]
	v_mad_u64_u32 v[36:37], s[48:49], v63, s33, v[10:11]
	v_mad_u64_u32 v[38:39], s[48:49], v62, s33, v[10:11]
	v_mad_u64_u32 v[40:41], s[48:49], v65, s33, v[10:11]
	v_mad_u64_u32 v[42:43], s[48:49], v64, s33, v[10:11]
	v_mad_u64_u32 v[44:45], s[48:49], v67, s33, v[10:11]
	v_mad_u64_u32 v[46:47], s[48:49], v66, s33, v[10:11]
	v_mad_u64_u32 v[48:49], s[48:49], v69, s33, v[10:11]
	v_mad_u64_u32 v[50:51], s[48:49], v68, s33, v[10:11]
	v_mad_u64_u32 v[52:53], s[48:49], v71, s33, v[10:11]
	v_mad_u64_u32 v[54:55], s[48:49], v70, s33, v[10:11]
	v_mad_u64_u32 v[56:57], s[48:49], v73, s33, v[10:11]
	v_mad_u64_u32 v[58:59], s[48:49], v72, s33, v[10:11]
	s_lshl_b32 s47, s25, 1
	s_lshl_b32 s48, s20, 1
	v_or_b32_e32 v112, s47, v1
	v_or_b32_e32 v113, s48, v8
	s_add_i32 s49, s47, 4
	s_add_i32 s50, s48, 4
	s_add_i32 s51, s47, 8
	s_add_i32 s52, s48, 8
	s_add_i32 s53, s47, 12
	s_add_i32 s54, s48, 12
	s_add_i32 s55, s47, 16
	s_add_i32 s60, s48, 16
	s_add_i32 s61, s47, 20
	s_add_i32 s62, s48, 20
	s_add_i32 s63, s47, 24
	s_add_i32 s64, s48, 24
	s_add_i32 s47, s47, 28
	s_add_i32 s48, s48, 28
	v_add_u32_e32 v110, s26, v113
	v_or_b32_e32 v144, s49, v1
	v_or_b32_e32 v145, s50, v8
	v_or_b32_e32 v146, s51, v1
	v_or_b32_e32 v147, s52, v8
	v_or_b32_e32 v148, s53, v1
	v_or_b32_e32 v149, s54, v8
	v_or_b32_e32 v150, s55, v1
	v_or_b32_e32 v151, s60, v8
	v_or_b32_e32 v152, s61, v1
	v_or_b32_e32 v153, s62, v8
	v_or_b32_e32 v154, s63, v1
	v_or_b32_e32 v155, s64, v8
	v_or_b32_e32 v156, s47, v1
	v_or_b32_e32 v157, s48, v8
	v_add_u32_e32 v114, s21, v112
	v_mad_i64_i32 v[110:111], s[48:49], v110, s31, v[4:5]
	v_add_u32_e32 v118, s21, v144
	v_add_u32_e32 v116, s26, v145
	v_add_u32_e32 v122, s21, v146
	v_add_u32_e32 v120, s26, v147
	v_add_u32_e32 v126, s21, v148
	v_add_u32_e32 v124, s26, v149
	v_add_u32_e32 v130, s21, v150
	v_add_u32_e32 v128, s26, v151
	v_add_u32_e32 v134, s21, v152
	v_add_u32_e32 v132, s26, v153
	v_add_u32_e32 v138, s21, v154
	v_add_u32_e32 v136, s26, v155
	v_add_u32_e32 v142, s21, v156
	v_add_u32_e32 v140, s26, v157
	v_mad_i64_i32 v[114:115], s[48:49], v114, s31, v[4:5]
	v_mad_i64_i32 v[116:117], s[48:49], v116, s31, v[4:5]
	v_mad_i64_i32 v[118:119], s[48:49], v118, s31, v[4:5]
	v_mad_i64_i32 v[120:121], s[48:49], v120, s31, v[4:5]
	v_mad_i64_i32 v[122:123], s[48:49], v122, s31, v[4:5]
	v_mad_i64_i32 v[124:125], s[48:49], v124, s31, v[4:5]
	v_mad_i64_i32 v[126:127], s[48:49], v126, s31, v[4:5]
	v_mad_i64_i32 v[128:129], s[48:49], v128, s31, v[4:5]
	v_mad_i64_i32 v[130:131], s[48:49], v130, s31, v[4:5]
	v_mad_i64_i32 v[132:133], s[48:49], v132, s31, v[4:5]
	v_mad_i64_i32 v[134:135], s[48:49], v134, s31, v[4:5]
	v_mad_i64_i32 v[136:137], s[48:49], v136, s31, v[4:5]
	v_mad_i64_i32 v[138:139], s[48:49], v138, s31, v[4:5]
	v_mad_i64_i32 v[140:141], s[48:49], v140, s31, v[4:5]
	v_mad_i64_i32 v[142:143], s[48:49], v142, s31, v[4:5]
	global_load_dword v158, v[110:111], off
	global_load_dword v159, v[114:115], off
	global_load_dword v160, v[116:117], off
	global_load_dword v161, v[118:119], off
	global_load_dword v162, v[120:121], off
	global_load_dword v163, v[122:123], off
	global_load_dword v164, v[124:125], off
	global_load_dword v165, v[126:127], off
	global_load_dword v166, v[128:129], off
	global_load_dword v167, v[130:131], off
	global_load_dword v168, v[132:133], off
	global_load_dword v169, v[134:135], off
	global_load_dword v170, v[136:137], off
	global_load_dword v171, v[138:139], off
	global_load_dword v172, v[140:141], off
	global_load_dword v173, v[142:143], off
	s_add_i32 s20, s20, 16
	s_add_i32 s25, s25, 16
	s_add_i32 s27, s27, -16
	v_mad_u64_u32 v[110:111], s[48:49], v113, s33, v[10:11]
	s_cmp_lg_u32 s27, 0
	v_mad_u64_u32 v[114:115], s[48:49], v112, s33, v[10:11]
	v_mad_u64_u32 v[116:117], s[48:49], v145, s33, v[10:11]
	v_mad_u64_u32 v[118:119], s[48:49], v144, s33, v[10:11]
	v_mad_u64_u32 v[120:121], s[48:49], v147, s33, v[10:11]
	v_mad_u64_u32 v[122:123], s[48:49], v146, s33, v[10:11]
	v_mad_u64_u32 v[124:125], s[48:49], v149, s33, v[10:11]
	v_mad_u64_u32 v[126:127], s[48:49], v148, s33, v[10:11]
	v_mad_u64_u32 v[128:129], s[48:49], v151, s33, v[10:11]
	v_mad_u64_u32 v[130:131], s[48:49], v150, s33, v[10:11]
	v_mad_u64_u32 v[132:133], s[48:49], v153, s33, v[10:11]
	v_mad_u64_u32 v[134:135], s[48:49], v152, s33, v[10:11]
	v_mad_u64_u32 v[136:137], s[48:49], v155, s33, v[10:11]
	v_mad_u64_u32 v[138:139], s[48:49], v154, s33, v[10:11]
	v_mad_u64_u32 v[140:141], s[48:49], v157, s33, v[10:11]
	v_mad_u64_u32 v[142:143], s[48:49], v156, s33, v[10:11]
	s_waitcnt vmcnt(16)
	ds_write_b32 v6, v74
	s_waitcnt vmcnt(30)
	ds_write_b32 v30, v75
	s_waitcnt vmcnt(29)
	ds_write_b32 v32, v76
	s_waitcnt vmcnt(28)
	ds_write_b32 v34, v77
	s_waitcnt vmcnt(27)
	ds_write_b32 v36, v78
	s_waitcnt vmcnt(26)
	ds_write_b32 v38, v79
	s_waitcnt vmcnt(25)
	ds_write_b32 v40, v80
	s_waitcnt vmcnt(24)
	ds_write_b32 v42, v81
	s_waitcnt vmcnt(23)
	ds_write_b32 v44, v82
	s_waitcnt vmcnt(22)
	ds_write_b32 v46, v83
	s_waitcnt vmcnt(21)
	ds_write_b32 v48, v84
	s_waitcnt vmcnt(20)
	ds_write_b32 v50, v85
	s_waitcnt vmcnt(19)
	ds_write_b32 v52, v86
	s_waitcnt vmcnt(18)
	ds_write_b32 v54, v87
	s_waitcnt vmcnt(17)
	ds_write_b32 v56, v88
	s_waitcnt vmcnt(16)
	ds_write_b32 v58, v89
	s_waitcnt vmcnt(0)
	ds_write_b32 v110, v158
	s_waitcnt vmcnt(14)
	ds_write_b32 v114, v159
	s_waitcnt vmcnt(13)
	ds_write_b32 v116, v160
	s_waitcnt vmcnt(12)
	ds_write_b32 v118, v161
	s_waitcnt vmcnt(11)
	ds_write_b32 v120, v162
	s_waitcnt vmcnt(10)
	ds_write_b32 v122, v163
	s_waitcnt vmcnt(9)
	ds_write_b32 v124, v164
	s_waitcnt vmcnt(8)
	ds_write_b32 v126, v165
	s_waitcnt vmcnt(7)
	ds_write_b32 v128, v166
	s_waitcnt vmcnt(6)
	ds_write_b32 v130, v167
	s_waitcnt vmcnt(5)
	ds_write_b32 v132, v168
	s_waitcnt vmcnt(4)
	ds_write_b32 v134, v169
	s_waitcnt vmcnt(3)
	ds_write_b32 v136, v170
	s_waitcnt vmcnt(2)
	ds_write_b32 v138, v171
	s_waitcnt vmcnt(1)
	ds_write_b32 v140, v172
	s_waitcnt vmcnt(0)
	ds_write_b32 v142, v173

.LBB0_401:
	s_lshl_b32 s42, s23, 1
	s_lshl_b32 s43, s27, 1
	v_or_b32_e32 v11, s42, v1
	v_or_b32_e32 v29, s43, v8
	s_add_i32 s44, s42, 4
	s_add_i32 s45, s43, 4
	s_add_i32 s46, s42, 8
	s_add_i32 s47, s43, 8
	s_add_i32 s48, s42, 12
	s_add_i32 s49, s43, 12
	s_add_i32 s50, s42, 16
	s_add_i32 s51, s43, 16
	s_add_i32 s52, s42, 20
	s_add_i32 s53, s43, 20
	s_add_i32 s54, s42, 24
	s_add_i32 s55, s43, 24
	s_add_i32 s42, s42, 28
	s_add_i32 s43, s43, 28
	v_add_u32_e32 v32, s22, v29
	v_or_b32_e32 v62, s44, v1
	v_or_b32_e32 v63, s45, v8
	v_or_b32_e32 v64, s46, v1
	v_or_b32_e32 v65, s47, v8
	v_or_b32_e32 v66, s48, v1
	v_or_b32_e32 v67, s49, v8
	v_or_b32_e32 v68, s50, v1
	v_or_b32_e32 v69, s51, v8
	v_or_b32_e32 v70, s52, v1
	v_or_b32_e32 v71, s53, v8
	v_or_b32_e32 v72, s54, v1
	v_or_b32_e32 v73, s55, v8
	v_or_b32_e32 v74, s42, v1
	v_or_b32_e32 v75, s43, v8
	v_add_u32_e32 v6, s21, v11
	v_ashrrev_i32_e32 v33, 31, v32
	v_add_u32_e32 v34, s21, v62
	v_add_u32_e32 v36, s22, v63
	v_add_u32_e32 v38, s21, v64
	v_add_u32_e32 v40, s22, v65
	v_add_u32_e32 v42, s21, v66
	v_add_u32_e32 v44, s22, v67
	v_add_u32_e32 v46, s21, v68
	v_add_u32_e32 v48, s22, v69
	v_add_u32_e32 v50, s21, v70
	v_add_u32_e32 v52, s22, v71
	v_add_u32_e32 v54, s21, v72
	v_add_u32_e32 v56, s22, v73
	v_add_u32_e32 v58, s21, v74
	v_add_u32_e32 v60, s22, v75
	v_ashrrev_i32_e32 v7, 31, v6
	v_lshlrev_b64 v[32:33], 12, v[32:33]
	v_ashrrev_i32_e32 v37, 31, v36
	v_ashrrev_i32_e32 v35, 31, v34
	v_ashrrev_i32_e32 v41, 31, v40
	v_ashrrev_i32_e32 v39, 31, v38
	v_ashrrev_i32_e32 v45, 31, v44
	v_ashrrev_i32_e32 v43, 31, v42
	v_ashrrev_i32_e32 v49, 31, v48
	v_ashrrev_i32_e32 v47, 31, v46
	v_ashrrev_i32_e32 v53, 31, v52
	v_ashrrev_i32_e32 v51, 31, v50
	v_ashrrev_i32_e32 v57, 31, v56
	v_ashrrev_i32_e32 v55, 31, v54
	v_ashrrev_i32_e32 v61, 31, v60
	v_ashrrev_i32_e32 v59, 31, v58
	v_lshlrev_b64 v[6:7], 12, v[6:7]
	v_lshl_add_u64 v[32:33], v[4:5], 0, v[32:33]
	v_lshlrev_b64 v[34:35], 12, v[34:35]
	v_lshlrev_b64 v[36:37], 12, v[36:37]
	v_lshlrev_b64 v[38:39], 12, v[38:39]
	v_lshlrev_b64 v[40:41], 12, v[40:41]
	v_lshlrev_b64 v[42:43], 12, v[42:43]
	v_lshlrev_b64 v[44:45], 12, v[44:45]
	v_lshlrev_b64 v[46:47], 12, v[46:47]
	v_lshlrev_b64 v[48:49], 12, v[48:49]
	v_lshlrev_b64 v[50:51], 12, v[50:51]
	v_lshlrev_b64 v[52:53], 12, v[52:53]
	v_lshlrev_b64 v[54:55], 12, v[54:55]
	v_lshlrev_b64 v[56:57], 12, v[56:57]
	v_lshlrev_b64 v[58:59], 12, v[58:59]
	v_lshlrev_b64 v[60:61], 12, v[60:61]
	v_lshl_add_u64 v[6:7], v[4:5], 0, v[6:7]
	v_lshl_add_u64 v[36:37], v[4:5], 0, v[36:37]
	v_lshl_add_u64 v[34:35], v[4:5], 0, v[34:35]
	v_lshl_add_u64 v[40:41], v[4:5], 0, v[40:41]
	v_lshl_add_u64 v[38:39], v[4:5], 0, v[38:39]
	v_lshl_add_u64 v[44:45], v[4:5], 0, v[44:45]
	v_lshl_add_u64 v[42:43], v[4:5], 0, v[42:43]
	v_lshl_add_u64 v[48:49], v[4:5], 0, v[48:49]
	v_lshl_add_u64 v[46:47], v[4:5], 0, v[46:47]
	v_lshl_add_u64 v[52:53], v[4:5], 0, v[52:53]
	v_lshl_add_u64 v[50:51], v[4:5], 0, v[50:51]
	v_lshl_add_u64 v[56:57], v[4:5], 0, v[56:57]
	v_lshl_add_u64 v[54:55], v[4:5], 0, v[54:55]
	v_lshl_add_u64 v[60:61], v[4:5], 0, v[60:61]
	v_lshl_add_u64 v[58:59], v[4:5], 0, v[58:59]
	global_load_dword v76, v[32:33], off
	global_load_dword v77, v[6:7], off
	global_load_dword v78, v[36:37], off
	global_load_dword v79, v[34:35], off
	global_load_dword v80, v[40:41], off
	global_load_dword v81, v[38:39], off
	global_load_dword v82, v[44:45], off
	global_load_dword v83, v[42:43], off
	global_load_dword v84, v[48:49], off
	global_load_dword v85, v[46:47], off
	global_load_dword v86, v[52:53], off
	global_load_dword v87, v[50:51], off
	global_load_dword v88, v[56:57], off
	global_load_dword v89, v[54:55], off
	global_load_dword v90, v[60:61], off
	global_load_dword v91, v[58:59], off
	s_add_i32 s27, s27, 16
	s_add_i32 s23, s23, 16
	s_add_i32 s41, s41, -16
	v_mad_u64_u32 v[6:7], s[42:43], v29, s33, v[10:11]
	s_cmp_lg_u32 s41, 0
	v_mad_u64_u32 v[32:33], s[42:43], v11, s33, v[10:11]
	v_mad_u64_u32 v[34:35], s[42:43], v63, s33, v[10:11]
	v_mad_u64_u32 v[36:37], s[42:43], v62, s33, v[10:11]
	v_mad_u64_u32 v[38:39], s[42:43], v65, s33, v[10:11]
	v_mad_u64_u32 v[40:41], s[42:43], v64, s33, v[10:11]
	v_mad_u64_u32 v[42:43], s[42:43], v67, s33, v[10:11]
	v_mad_u64_u32 v[44:45], s[42:43], v66, s33, v[10:11]
	v_mad_u64_u32 v[46:47], s[42:43], v69, s33, v[10:11]
	v_mad_u64_u32 v[48:49], s[42:43], v68, s33, v[10:11]
	v_mad_u64_u32 v[50:51], s[42:43], v71, s33, v[10:11]
	v_mad_u64_u32 v[52:53], s[42:43], v70, s33, v[10:11]
	v_mad_u64_u32 v[54:55], s[42:43], v73, s33, v[10:11]
	v_mad_u64_u32 v[56:57], s[42:43], v72, s33, v[10:11]
	v_mad_u64_u32 v[58:59], s[42:43], v75, s33, v[10:11]
	v_mad_u64_u32 v[60:61], s[42:43], v74, s33, v[10:11]
	s_lshl_b32 s42, s23, 1
	s_lshl_b32 s43, s27, 1
	v_or_b32_e32 v112, s42, v1
	v_or_b32_e32 v113, s43, v8
	s_add_i32 s44, s42, 4
	s_add_i32 s45, s43, 4
	s_add_i32 s46, s42, 8
	s_add_i32 s47, s43, 8
	s_add_i32 s48, s42, 12
	s_add_i32 s49, s43, 12
	s_add_i32 s50, s42, 16
	s_add_i32 s51, s43, 16
	s_add_i32 s52, s42, 20
	s_add_i32 s53, s43, 20
	s_add_i32 s54, s42, 24
	s_add_i32 s55, s43, 24
	s_add_i32 s42, s42, 28
	s_add_i32 s43, s43, 28
	v_add_u32_e32 v114, s22, v113
	v_or_b32_e32 v144, s44, v1
	v_or_b32_e32 v145, s45, v8
	v_or_b32_e32 v146, s46, v1
	v_or_b32_e32 v147, s47, v8
	v_or_b32_e32 v148, s48, v1
	v_or_b32_e32 v149, s49, v8
	v_or_b32_e32 v150, s50, v1
	v_or_b32_e32 v151, s51, v8
	v_or_b32_e32 v152, s52, v1
	v_or_b32_e32 v153, s53, v8
	v_or_b32_e32 v154, s54, v1
	v_or_b32_e32 v155, s55, v8
	v_or_b32_e32 v156, s42, v1
	v_or_b32_e32 v157, s43, v8
	v_add_u32_e32 v110, s21, v112
	v_ashrrev_i32_e32 v115, 31, v114
	v_add_u32_e32 v116, s21, v144
	v_add_u32_e32 v118, s22, v145
	v_add_u32_e32 v120, s21, v146
	v_add_u32_e32 v122, s22, v147
	v_add_u32_e32 v124, s21, v148
	v_add_u32_e32 v126, s22, v149
	v_add_u32_e32 v128, s21, v150
	v_add_u32_e32 v130, s22, v151
	v_add_u32_e32 v132, s21, v152
	v_add_u32_e32 v134, s22, v153
	v_add_u32_e32 v136, s21, v154
	v_add_u32_e32 v138, s22, v155
	v_add_u32_e32 v140, s21, v156
	v_add_u32_e32 v142, s22, v157
	v_ashrrev_i32_e32 v111, 31, v110
	v_lshlrev_b64 v[114:115], 12, v[114:115]
	v_ashrrev_i32_e32 v119, 31, v118
	v_ashrrev_i32_e32 v117, 31, v116
	v_ashrrev_i32_e32 v123, 31, v122
	v_ashrrev_i32_e32 v121, 31, v120
	v_ashrrev_i32_e32 v127, 31, v126
	v_ashrrev_i32_e32 v125, 31, v124
	v_ashrrev_i32_e32 v131, 31, v130
	v_ashrrev_i32_e32 v129, 31, v128
	v_ashrrev_i32_e32 v135, 31, v134
	v_ashrrev_i32_e32 v133, 31, v132
	v_ashrrev_i32_e32 v139, 31, v138
	v_ashrrev_i32_e32 v137, 31, v136
	v_ashrrev_i32_e32 v143, 31, v142
	v_ashrrev_i32_e32 v141, 31, v140
	v_lshlrev_b64 v[110:111], 12, v[110:111]
	v_lshl_add_u64 v[114:115], v[4:5], 0, v[114:115]
	v_lshlrev_b64 v[116:117], 12, v[116:117]
	v_lshlrev_b64 v[118:119], 12, v[118:119]
	v_lshlrev_b64 v[120:121], 12, v[120:121]
	v_lshlrev_b64 v[122:123], 12, v[122:123]
	v_lshlrev_b64 v[124:125], 12, v[124:125]
	v_lshlrev_b64 v[126:127], 12, v[126:127]
	v_lshlrev_b64 v[128:129], 12, v[128:129]
	v_lshlrev_b64 v[130:131], 12, v[130:131]
	v_lshlrev_b64 v[132:133], 12, v[132:133]
	v_lshlrev_b64 v[134:135], 12, v[134:135]
	v_lshlrev_b64 v[136:137], 12, v[136:137]
	v_lshlrev_b64 v[138:139], 12, v[138:139]
	v_lshlrev_b64 v[140:141], 12, v[140:141]
	v_lshlrev_b64 v[142:143], 12, v[142:143]
	v_lshl_add_u64 v[110:111], v[4:5], 0, v[110:111]
	v_lshl_add_u64 v[118:119], v[4:5], 0, v[118:119]
	v_lshl_add_u64 v[116:117], v[4:5], 0, v[116:117]
	v_lshl_add_u64 v[122:123], v[4:5], 0, v[122:123]
	v_lshl_add_u64 v[120:121], v[4:5], 0, v[120:121]
	v_lshl_add_u64 v[126:127], v[4:5], 0, v[126:127]
	v_lshl_add_u64 v[124:125], v[4:5], 0, v[124:125]
	v_lshl_add_u64 v[130:131], v[4:5], 0, v[130:131]
	v_lshl_add_u64 v[128:129], v[4:5], 0, v[128:129]
	v_lshl_add_u64 v[134:135], v[4:5], 0, v[134:135]
	v_lshl_add_u64 v[132:133], v[4:5], 0, v[132:133]
	v_lshl_add_u64 v[138:139], v[4:5], 0, v[138:139]
	v_lshl_add_u64 v[136:137], v[4:5], 0, v[136:137]
	v_lshl_add_u64 v[142:143], v[4:5], 0, v[142:143]
	v_lshl_add_u64 v[140:141], v[4:5], 0, v[140:141]
	global_load_dword v158, v[114:115], off
	global_load_dword v159, v[110:111], off
	global_load_dword v160, v[118:119], off
	global_load_dword v161, v[116:117], off
	global_load_dword v162, v[122:123], off
	global_load_dword v163, v[120:121], off
	global_load_dword v164, v[126:127], off
	global_load_dword v165, v[124:125], off
	global_load_dword v166, v[130:131], off
	global_load_dword v167, v[128:129], off
	global_load_dword v168, v[134:135], off
	global_load_dword v169, v[132:133], off
	global_load_dword v170, v[138:139], off
	global_load_dword v171, v[136:137], off
	global_load_dword v172, v[142:143], off
	global_load_dword v173, v[140:141], off
	s_add_i32 s27, s27, 16
	s_add_i32 s23, s23, 16
	s_add_i32 s41, s41, -16
	v_mad_u64_u32 v[110:111], s[42:43], v113, s33, v[10:11]
	s_cmp_lg_u32 s41, 0
	v_mad_u64_u32 v[114:115], s[42:43], v112, s33, v[10:11]
	v_mad_u64_u32 v[116:117], s[42:43], v145, s33, v[10:11]
	v_mad_u64_u32 v[118:119], s[42:43], v144, s33, v[10:11]
	v_mad_u64_u32 v[120:121], s[42:43], v147, s33, v[10:11]
	v_mad_u64_u32 v[122:123], s[42:43], v146, s33, v[10:11]
	v_mad_u64_u32 v[124:125], s[42:43], v149, s33, v[10:11]
	v_mad_u64_u32 v[126:127], s[42:43], v148, s33, v[10:11]
	v_mad_u64_u32 v[128:129], s[42:43], v151, s33, v[10:11]
	v_mad_u64_u32 v[130:131], s[42:43], v150, s33, v[10:11]
	v_mad_u64_u32 v[132:133], s[42:43], v153, s33, v[10:11]
	v_mad_u64_u32 v[134:135], s[42:43], v152, s33, v[10:11]
	v_mad_u64_u32 v[136:137], s[42:43], v155, s33, v[10:11]
	v_mad_u64_u32 v[138:139], s[42:43], v154, s33, v[10:11]
	v_mad_u64_u32 v[140:141], s[42:43], v157, s33, v[10:11]
	v_mad_u64_u32 v[142:143], s[42:43], v156, s33, v[10:11]
	s_waitcnt vmcnt(16)
	ds_write_b32 v6, v76
	s_waitcnt vmcnt(30)
	ds_write_b32 v32, v77
	s_waitcnt vmcnt(29)
	ds_write_b32 v34, v78
	s_waitcnt vmcnt(28)
	ds_write_b32 v36, v79
	s_waitcnt vmcnt(27)
	ds_write_b32 v38, v80
	s_waitcnt vmcnt(26)
	ds_write_b32 v40, v81
	s_waitcnt vmcnt(25)
	ds_write_b32 v42, v82
	s_waitcnt vmcnt(24)
	ds_write_b32 v44, v83
	s_waitcnt vmcnt(23)
	ds_write_b32 v46, v84
	s_waitcnt vmcnt(22)
	ds_write_b32 v48, v85
	s_waitcnt vmcnt(21)
	ds_write_b32 v50, v86
	s_waitcnt vmcnt(20)
	ds_write_b32 v52, v87
	s_waitcnt vmcnt(19)
	ds_write_b32 v54, v88
	s_waitcnt vmcnt(18)
	ds_write_b32 v56, v89
	s_waitcnt vmcnt(17)
	ds_write_b32 v58, v90
	s_waitcnt vmcnt(16)
	ds_write_b32 v60, v91
	s_waitcnt vmcnt(0)
	ds_write_b32 v110, v158
	s_waitcnt vmcnt(14)
	ds_write_b32 v114, v159
	s_waitcnt vmcnt(13)
	ds_write_b32 v116, v160
	s_waitcnt vmcnt(12)
	ds_write_b32 v118, v161
	s_waitcnt vmcnt(11)
	ds_write_b32 v120, v162
	s_waitcnt vmcnt(10)
	ds_write_b32 v122, v163
	s_waitcnt vmcnt(9)
	ds_write_b32 v124, v164
	s_waitcnt vmcnt(8)
	ds_write_b32 v126, v165
	s_waitcnt vmcnt(7)
	ds_write_b32 v128, v166
	s_waitcnt vmcnt(6)
	ds_write_b32 v130, v167
	s_waitcnt vmcnt(5)
	ds_write_b32 v132, v168
	s_waitcnt vmcnt(4)
	ds_write_b32 v134, v169
	s_waitcnt vmcnt(3)
	ds_write_b32 v136, v170
	s_waitcnt vmcnt(2)
	ds_write_b32 v138, v171
	s_waitcnt vmcnt(1)
	ds_write_b32 v140, v172
	s_waitcnt vmcnt(0)
	ds_write_b32 v142, v173
